# attention: first two K ds_reads of each step hoisted above the CV head code; trims
# baseline (speedup 1.0000x reference)
; #define AT_SWRITE(b, i) do { *(bf16x8*)(V_lds + (b) * SHM_V + vst0) = sr_[i].vs0; *(bf16x8*)(V_lds + (b) * SHM_V + vst1) = sr_[i].vs1; *(bf16x8*)(K_lds + (b) * SHM_K + kst) = sr_[i].ks0; } while (0)
; DI void qkt(f32x16& p0, f32x16& p1, const char* Ks, const bf16x8* qr, const f32x16& negm, int r32, int hi) {
; #pragma unroll
;     for (int d0 = 0; d0 < 4; ++d0) { const int cb = (d0 * 16 + hi * 8) * 2;
;         const bf16x8 b0 = *reinterpret_cast<const bf16x8*>(Ks + AT_KSWZ(r32, cb));
;         const bf16x8 b1 = *reinterpret_cast<const bf16x8*>(Ks + AT_KSWZ(32 + r32, cb));
;         p0 = __builtin_amdgcn_mfma_f32_32x32x16_bf16(b0, qr[d0], d0 == 0 ? negm : p0, 0, 0, 0);
;         p1 = __builtin_amdgcn_mfma_f32_32x32x16_bf16(b1, qr[d0], d0 == 0 ? negm : p1, 0, 0, 0); }
; }
; DI void attn_pass(const Frame& F, CvRide& cv, const bf16_t* __restrict__ Qb, const bf16_t* __restrict__ Kh, const bf16_t* __restrict__ Vh, char* lds, f32x16 (&o)[4], float& l_out, const int wave_s) {
;     ...
;     f32x16 pA0, pA1, pB0, pB1; float alA, alB; bf16x8 pa0, pa1, pa2, pa3; constexpr int NT = S / 64;
;     constexpr int SE = 0;
;     {
;         bf16x8 v10 = *reinterpret_cast<const bf16x8*>(&Vh[(size_t)(64 + sr) * 128 + sc]), v11 = *reinterpret_cast<const bf16x8*>(&Vh[(size_t)(96 + sr) * 128 + sc]);
;         bf16x8 k10 = *reinterpret_cast<const bf16x8*>(&Kh[(size_t)(64 + kr) * 64 + (tid & 7) * 8]);
;         AT_SLOAD(SE, 0); asm volatile("s_waitcnt vmcnt(0)" ::: "memory");
;         __syncthreads();
;         AT_SWRITE(0, SE);
;         *(bf16x8*)(V_lds + SHM_V + vst0) = v10; *(bf16x8*)(V_lds + SHM_V + vst1) = v11; *(bf16x8*)(K_lds + SHM_K + kst) = k10;
;         __syncthreads();
;     }
;     qkt(pA0, pA1, K_lds, qr, negm, r32, hi); partialSM(pA0, pA1, m_ref, negm, alA);
;     int s_prev = 0, s_cur = 1, s_next = 2;
.LBB4_692:
	s_lshl_b32 s92, s65, 13
	v_add_u32_e32 v68, s92, v204
	ds_read_b128 v[64:67], v68 offset:49152
	ds_read_b128 v[68:71], v68 offset:53248
	s_cmp_lg_u32 s26, 0
	s_mov_b32 s66, s65
	s_cselect_b64 s[2:3], -1, 0
	s_cmp_eq_u32 s26, 0
	s_mov_b32 s65, s34
	s_cbranch_scc1 .LBB4_694
	s_andn2_b32 s26, 1, s58
	s_mulk_i32 s26, 0x1100
	v_add_u32_e32 v252, s26, v190
	ds_read2_b32 v[184:185], v252 offset1:1

; DI void finishSM(f32x16& p0, f32x16& p1, float alpha, float& l_reg, bf16x8& pa0, bf16x8& pa1, bf16x8& pa2, bf16x8& pa3) {
; #pragma unroll
;     for (int r = 0; r < 16; ++r) p1[r] = __builtin_amdgcn_exp2f(p1[r]);
;     float ps = 0;
; #pragma unroll
;     for (int r = 0; r < 16; ++r) ps += p0[r];
; #pragma unroll
;     for (int r = 0; r < 16; ++r) ps += p1[r];
;     { auto rr = __builtin_amdgcn_permlane32_swap(__float_as_uint(ps), __float_as_uint(ps), false, false); ps = __uint_as_float(rr[0]) + __uint_as_float(rr[1]); }
;     l_reg = l_reg * alpha + ps;
;     ...
;     AT_PK4(p0, 0, pa0); AT_PK4(p0, 8, pa1); AT_PK4(p1, 0, pa2); AT_PK4(p1, 8, pa3);
;     ...
; }
; DI void qkt(f32x16& p0, f32x16& p1, const char* Ks, const bf16x8* qr, const f32x16& negm, int r32, int hi) {
; #pragma unroll
;     for (int d0 = 0; d0 < 4; ++d0) { const int cb = (d0 * 16 + hi * 8) * 2;
;         const bf16x8 b0 = *reinterpret_cast<const bf16x8*>(Ks + AT_KSWZ(r32, cb));
;         const bf16x8 b1 = *reinterpret_cast<const bf16x8*>(Ks + AT_KSWZ(32 + r32, cb));
;         p0 = __builtin_amdgcn_mfma_f32_32x32x16_bf16(b0, qr[d0], d0 == 0 ? negm : p0, 0, 0, 0);
;         p1 = __builtin_amdgcn_mfma_f32_32x32x16_bf16(b1, qr[d0], d0 == 0 ? negm : p1, 0, 0, 0); }
; }
; DI void attn_pass(const Frame& F, CvRide& cv, const bf16_t* __restrict__ Qb, const bf16_t* __restrict__ Kh, const bf16_t* __restrict__ Vh, char* lds, f32x16 (&o)[4], float& l_out, const int wave_s) {
;     ...
;     const unsigned cv_ldo = (unsigned)(((tid >> 4) * 2 * 2048 + (tid & 15) * 4) * 4), cv_sto = (unsigned)((tid >> 3) * 2048 + 8 * (tid & 7));
;     const int cv_lw = OFF_CV + (4 * (tid & 15)) * 68 + 2 * (tid >> 4), cv_lr = OFF_CV + (tid >> 3) * 68 + 8 * (tid & 7);
;     f32x4 cvA = f32x4{}, cvB = f32x4{}; unsigned cvr0 = 0, cvr1 = 0;
.LBB4_701:
	s_lshl_b32 s26, s58, 8
	s_and_b32 s26, s26, 0x1f00
	s_add_u32 s74, s12, s26
	s_addc_u32 s75, s13, 0
	s_add_u32 s76, s74, 0x2000
	s_addc_u32 s77, s75, 0
	v_mov_b32_e32 v252, v209
	global_load_dwordx4 v[160:163], v252, s[74:75] nt
	global_load_dwordx4 v[164:167], v252, s[76:77] nt
.LBB4_702:
	s_lshl_b32 s26, s66, 13
	s_add_i32 s26, s26, 0
	v_add_u32_e32 v72, s26, v205
	v_add_u32_e32 v112, s26, v206
	v_add_u32_e32 v180, s26, v207
	s_waitcnt lgkmcnt(1)
	v_mfma_f32_32x32x16_bf16 v[128:143], v[64:67], v[156:159], v[80:95]
	ds_read_b128 v[64:67], v72 offset:49152
	ds_read_b128 v[72:75], v72 offset:53248
	ds_read_b128 v[76:79], v112 offset:49152
	ds_read_b128 v[220:223], v112 offset:53248
	v_exp_f32_e32 v186, v97
	v_exp_f32_e32 v213, v98
	v_exp_f32_e32 v214, v99
	v_exp_f32_e32 v219, v100
	v_exp_f32_e32 v228, v101
	s_waitcnt lgkmcnt(4)
	v_mfma_f32_32x32x16_bf16 v[112:127], v[68:71], v[156:159], v[80:95]
	ds_read_b128 v[68:71], v180 offset:49152
	ds_read_b128 v[224:227], v180 offset:53248
	v_exp_f32_e32 v180, v96
	v_cvt_pk_bf16_f32 v96, v216, v218
	v_cvt_pk_bf16_f32 v97, v179, v217
	v_cvt_pk_bf16_f32 v98, v177, v215
	v_cvt_pk_bf16_f32 v99, v176, v178
	s_waitcnt lgkmcnt(4)
	v_mfma_f32_32x32x16_bf16 v[112:127], v[72:75], v[152:155], v[112:127]
	v_add_f32_e32 v75, 0, v216
	v_add_f32_e32 v75, v218, v75
	v_add_f32_e32 v75, v179, v75
	v_add_f32_e32 v75, v217, v75
	v_add_f32_e32 v75, v177, v75
	v_add_f32_e32 v75, v215, v75
	v_add_f32_e32 v75, v176, v75
	v_mfma_f32_32x32x16_bf16 v[128:143], v[64:67], v[152:155], v[128:143]
	v_add_f32_e32 v75, v178, v75
	v_add_f32_e32 v75, v173, v75
	v_add_f32_e32 v75, v175, v75
	v_add_f32_e32 v75, v171, v75
	v_add_f32_e32 v75, v174, v75
	v_add_f32_e32 v75, v169, v75
	v_add_f32_e32 v75, v172, v75
	s_waitcnt lgkmcnt(3)
	v_mfma_f32_32x32x16_bf16 v[128:143], v[76:79], v[148:151], v[128:143]
	v_add_f32_e32 v75, v168, v75
	v_add_f32_e32 v75, v170, v75
	v_add_f32_e32 v75, v180, v75
	v_add_f32_e32 v75, v186, v75
	v_exp_f32_e32 v64, v102
	v_exp_f32_e32 v65, v103
	v_exp_f32_e32 v66, v104
	s_waitcnt lgkmcnt(2)
	v_mfma_f32_32x32x16_bf16 v[112:127], v[220:223], v[148:151], v[112:127]
	v_exp_f32_e32 v67, v105
	v_exp_f32_e32 v105, v106
	v_exp_f32_e32 v106, v107
	v_exp_f32_e32 v107, v108
	v_exp_f32_e32 v72, v109
	v_exp_f32_e32 v73, v110
	v_exp_f32_e32 v74, v111
	s_waitcnt lgkmcnt(1)
	v_mfma_f32_32x32x16_bf16 v[128:143], v[68:71], v[144:147], v[128:143]
	v_add_f32_e32 v68, v213, v75
	v_add_f32_e32 v68, v214, v68
	v_add_f32_e32 v68, v219, v68
	v_add_f32_e32 v68, v228, v68
	v_add_f32_e32 v68, v64, v68
	v_add_f32_e32 v68, v65, v68
	v_add_f32_e32 v68, v66, v68
	v_add_f32_e32 v68, v67, v68
	s_waitcnt lgkmcnt(0)
	v_mfma_f32_32x32x16_bf16 v[112:127], v[224:227], v[144:147], v[112:127]
	v_add_f32_e32 v68, v105, v68
	v_add_f32_e32 v68, v106, v68
	v_add_f32_e32 v68, v107, v68
	v_add_f32_e32 v68, v72, v68
	v_add_f32_e32 v68, v73, v68
	v_add_f32_e32 v183, v74, v68
	v_mov_b32_e32 v212, v183
	v_cvt_pk_bf16_f32 v108, v173, v175
	v_cvt_pk_bf16_f32 v109, v171, v174
	v_cvt_pk_bf16_f32 v110, v169, v172
	v_cvt_pk_bf16_f32 v111, v168, v170
	v_cvt_pk_bf16_f32 v100, v180, v186
	v_cvt_pk_bf16_f32 v101, v213, v214
	v_cvt_pk_bf16_f32 v102, v219, v228
	v_cvt_pk_bf16_f32 v103, v64, v65
	v_cvt_pk_bf16_f32 v104, v66, v67
	v_cvt_pk_bf16_f32 v105, v105, v106
	v_cvt_pk_bf16_f32 v106, v107, v72
	v_cvt_pk_bf16_f32 v107, v73, v74
	s_nop 1
	v_permlane32_swap_b32_e32 v183, v212
	v_permlane32_swap_b32_e32 v96, v98
	v_permlane32_swap_b32_e32 v97, v99
	v_permlane32_swap_b32_e32 v108, v110
	v_permlane32_swap_b32_e32 v109, v111
	v_permlane32_swap_b32_e32 v100, v102
	v_permlane32_swap_b32_e32 v101, v103
	v_permlane32_swap_b32_e32 v104, v106
	v_permlane32_swap_b32_e32 v105, v107
	s_add_u32 s74, s46, s28
	s_addc_u32 s75, s47, s29
	s_add_u32 s78, s74, 0x23808000
	s_addc_u32 s79, s75, 0
	s_add_u32 s80, s74, 0x2380a000
	s_addc_u32 s81, s75, 0
	s_add_u32 s76, s46, s30
	s_addc_u32 s77, s47, s31
	s_add_u32 s82, s76, 0x21804000
	s_addc_u32 s83, s77, 0
	v_mov_b32_e32 v64, v198
	v_mov_b32_e32 v65, v197
	global_load_dwordx4 v[176:179], v65, s[78:79]
	global_load_dwordx4 v[172:175], v65, s[80:81]
	global_load_dwordx4 v[168:171], v64, s[82:83]
	s_andn2_b64 vcc, exec, s[2:3]
	s_cbranch_vccnz .LBB4_704
	s_mov_b64 s[2:3], s[8:9]
	v_mov_b32_e32 v64, v189
	global_store_dwordx2 v64, v[184:185], s[2:3] nt

; #define AT_SBAR() __builtin_amdgcn_sched_barrier(0)
; template <int OFF> DI s16x4 tr_read(int vb) { s16x4 r; asm volatile("ds_read_b64_tr_b16 %0, %1 offset:%2" : "=&v"(r) : "v"(vb), "i"(OFF) : "memory"); return r; }
; template <int D0> DI void pv_one(f32x16& od, int vb, bf16x8 pa0, bf16x8 pa1, bf16x8 pa2, bf16x8 pa3) {
;     const s16x4 l0 = tr_read<v_rd_off(D0, 0, 0)>(vb), h0 = tr_read<v_rd_off(D0, 0, 1)>(vb), l1 = tr_read<v_rd_off(D0, 1, 0)>(vb), h1 = tr_read<v_rd_off(D0, 1, 1)>(vb);
;     const s16x4 l2 = tr_read<v_rd_off(D0, 2, 0)>(vb), h2 = tr_read<v_rd_off(D0, 2, 1)>(vb), l3 = tr_read<v_rd_off(D0, 3, 0)>(vb), h3 = tr_read<v_rd_off(D0, 3, 1)>(vb);
;     asm volatile("s_waitcnt lgkmcnt(0)" ::: "memory"); AT_SBAR();
;     ...
;     od = __builtin_amdgcn_mfma_f32_32x32x16_bf16(AT_PK(l0, h0), pa0, od, 0, 0, 0);
;     od = __builtin_amdgcn_mfma_f32_32x32x16_bf16(AT_PK(l1, h1), pa1, od, 0, 0, 0);
;     od = __builtin_amdgcn_mfma_f32_32x32x16_bf16(AT_PK(l2, h2), pa2, od, 0, 0, 0);
;     od = __builtin_amdgcn_mfma_f32_32x32x16_bf16(AT_PK(l3, h3), pa3, od, 0, 0, 0);
;     ...
; }
; DI void attn_pass(const Frame& F, CvRide& cv, const bf16_t* __restrict__ Qb, const bf16_t* __restrict__ Kh, const bf16_t* __restrict__ Vh, char* lds, f32x16 (&o)[4], float& l_out, const int wave_s) {
;     ...
;     const unsigned cv_ldo = (unsigned)(((tid >> 4) * 2 * 2048 + (tid & 15) * 4) * 4), cv_sto = (unsigned)((tid >> 3) * 2048 + 8 * (tid & 7));
;     const int cv_lw = OFF_CV + (4 * (tid & 15)) * 68 + 2 * (tid >> 4), cv_lr = OFF_CV + (tid >> 3) * 68 + 8 * (tid & 7);
;     f32x4 cvA = f32x4{}, cvB = f32x4{}; unsigned cvr0 = 0, cvr1 = 0;
.LBB4_706:
	ds_read_b64_tr_b16 v[214:215], v186 offset:0x600
	ds_read_b64_tr_b16 v[216:217], v186 offset:0xe00
	ds_read_b64_tr_b16 v[218:219], v186 offset:0x1600
	ds_read_b64_tr_b16 v[220:221], v186 offset:0x1e00
	ds_read_b64_tr_b16 v[222:223], v186 offset:0x2600
	ds_read_b64_tr_b16 v[224:225], v186 offset:0x2e00
	ds_read_b64_tr_b16 v[226:227], v186 offset:0x3600
	ds_read_b64_tr_b16 v[228:229], v186 offset:0x3e00
	s_waitcnt lgkmcnt(0)
	s_nop 0
	v_mfma_f32_32x32x16_bf16 v[0:15], v[214:217], v[96:99], v[0:15]
	s_lshl_b32 s2, s64, 14
	s_add_i32 s2, s2, 0
	s_lshl_b32 s3, s64, 13
	v_add_u32_e32 v96, s2, v200
	s_sub_i32 s78, s2, s3
	s_waitcnt vmcnt(0)
	v_add_u32_e32 v97, s2, v201
	v_mfma_f32_32x32x16_bf16 v[0:15], v[218:221], v[108:111], v[0:15]
	ds_write_b128 v96, v[176:179]
	v_add_u32_e32 v96, s78, v202
	ds_write_b128 v97, v[172:175]
	ds_write_b128 v96, v[168:171] offset:49152
	s_andn2_b64 s[2:3], exec, s[34:35]
	s_andn2_b64 vcc, exec, s[34:35]
	v_mfma_f32_32x32x16_bf16 v[0:15], v[222:225], v[100:103], v[0:15]
	v_mfma_f32_32x32x16_bf16 v[0:15], v[226:229], v[104:107], v[0:15]
	s_cbranch_vccnz .LBB4_711
	v_mul_f32_e32 v97, 0x44000000, v160
	v_mul_f32_e32 v98, 0x44000000, v164
	v_med3_f32 v97, v97, s62, v211
	v_med3_f32 v98, v98, s62, v211
	v_cvt_pk_fp8_f32 v99, v97, v98
	v_mul_f32_e32 v97, 0x44000000, v161
	v_mul_f32_e32 v98, 0x44000000, v165
	v_med3_f32 v97, v97, s62, v211
	v_med3_f32 v98, v98, s62, v211
	v_cvt_pk_fp8_f32 v100, v97, v98
	v_mul_f32_e32 v97, 0x44000000, v162
	v_mul_f32_e32 v98, 0x44000000, v166
	v_med3_f32 v97, v97, s62, v211
	v_med3_f32 v98, v98, s62, v211
	s_bitcmp1_b32 s58, 0
	v_cvt_pk_fp8_f32 v101, v97, v98
	v_mul_f32_e32 v97, 0x44000000, v163
	v_mul_f32_e32 v98, 0x44000000, v167
	s_cselect_b32 s8, 0x1100, 0
	v_med3_f32 v97, v97, s62, v211
	v_med3_f32 v98, v98, s62, v211
	v_cmp_eq_u32_e32 vcc, 0, v181
	v_add_u32_e32 v96, s8, v191
	v_cvt_pk_fp8_f32 v102, v97, v98
	s_and_b64 vcc, exec, vcc
	s_and_b32 s34, s58, 31
	ds_write_b16 v96, v99
	ds_write_b16 v96, v100 offset:68
	ds_write_b16 v96, v101 offset:136
	ds_write_b16 v96, v102 offset:204
	s_cbranch_vccnz .LBB4_735
	s_lshl_b32 s8, s34, 7
	s_lshl_b32 s9, s58, 6
	s_and_b32 s8, s8, 0xf00
	s_and_b32 s9, s9, 64
	s_or_b32 s26, s8, s9
	s_cbranch_execnz .LBB4_710

; #define AT_SWRITE(b, i) do { *(bf16x8*)(V_lds + (b) * SHM_V + vst0) = sr_[i].vs0; *(bf16x8*)(V_lds + (b) * SHM_V + vst1) = sr_[i].vs1; *(bf16x8*)(K_lds + (b) * SHM_K + kst) = sr_[i].ks0; } while (0)
; DI void attn_pass(const Frame& F, CvRide& cv, const bf16_t* __restrict__ Qb, const bf16_t* __restrict__ Kh, const bf16_t* __restrict__ Vh, char* lds, f32x16 (&o)[4], float& l_out, const int wave_s) {
;     ...
;     f32x16 pA0, pA1, pB0, pB1; float alA, alB; bf16x8 pa0, pa1, pa2, pa3; constexpr int NT = S / 64;
;     constexpr int SE = 0;
;     {
;         bf16x8 v10 = *reinterpret_cast<const bf16x8*>(&Vh[(size_t)(64 + sr) * 128 + sc]), v11 = *reinterpret_cast<const bf16x8*>(&Vh[(size_t)(96 + sr) * 128 + sc]);
;         bf16x8 k10 = *reinterpret_cast<const bf16x8*>(&Kh[(size_t)(64 + kr) * 64 + (tid & 7) * 8]);
;         AT_SLOAD(SE, 0); asm volatile("s_waitcnt vmcnt(0)" ::: "memory");
;         __syncthreads();
;         AT_SWRITE(0, SE);
;         *(bf16x8*)(V_lds + SHM_V + vst0) = v10; *(bf16x8*)(V_lds + SHM_V + vst1) = v11; *(bf16x8*)(K_lds + SHM_K + kst) = k10;
;         __syncthreads();
;     }
;     qkt(pA0, pA1, K_lds, qr, negm, r32, hi); partialSM(pA0, pA1, m_ref, negm, alA);
;     int s_prev = 0, s_cur = 1, s_next = 2;
.LBB4_713:
	s_and_b64 vcc, exec, s[2:3]
	s_waitcnt lgkmcnt(0)
	s_barrier
	v_add_u32_e32 v100, s78, v204
	ds_read_b128 v[96:99], v100 offset:49152
	ds_read_b128 v[168:171], v100 offset:53248
	s_cbranch_vccnz .LBB4_715
	s_andn2_b32 s26, 1, s58
	s_mulk_i32 s26, 0x1100
	v_add_u32_e32 v252, s26, v190
	ds_read2_b32 v[184:185], v252 offset1:1

; DI void finishSM(f32x16& p0, f32x16& p1, float alpha, float& l_reg, bf16x8& pa0, bf16x8& pa1, bf16x8& pa2, bf16x8& pa3) {
; #pragma unroll
;     for (int r = 0; r < 16; ++r) p1[r] = __builtin_amdgcn_exp2f(p1[r]);
;     float ps = 0;
; #pragma unroll
;     for (int r = 0; r < 16; ++r) ps += p0[r];
; #pragma unroll
;     for (int r = 0; r < 16; ++r) ps += p1[r];
;     { auto rr = __builtin_amdgcn_permlane32_swap(__float_as_uint(ps), __float_as_uint(ps), false, false); ps = __uint_as_float(rr[0]) + __uint_as_float(rr[1]); }
;     l_reg = l_reg * alpha + ps;
;     ...
;     AT_PK4(p0, 0, pa0); AT_PK4(p0, 8, pa1); AT_PK4(p1, 0, pa2); AT_PK4(p1, 8, pa3);
;     ...
; }
; DI void qkt(f32x16& p0, f32x16& p1, const char* Ks, const bf16x8* qr, const f32x16& negm, int r32, int hi) {
; #pragma unroll
;     for (int d0 = 0; d0 < 4; ++d0) { const int cb = (d0 * 16 + hi * 8) * 2;
;         const bf16x8 b0 = *reinterpret_cast<const bf16x8*>(Ks + AT_KSWZ(r32, cb));
;         const bf16x8 b1 = *reinterpret_cast<const bf16x8*>(Ks + AT_KSWZ(32 + r32, cb));
;         p0 = __builtin_amdgcn_mfma_f32_32x32x16_bf16(b0, qr[d0], d0 == 0 ? negm : p0, 0, 0, 0);
;         p1 = __builtin_amdgcn_mfma_f32_32x32x16_bf16(b1, qr[d0], d0 == 0 ? negm : p1, 0, 0, 0); }
; }
; DI void attn_pass(const Frame& F, CvRide& cv, const bf16_t* __restrict__ Qb, const bf16_t* __restrict__ Kh, const bf16_t* __restrict__ Vh, char* lds, f32x16 (&o)[4], float& l_out, const int wave_s) {
;     ...
;     const unsigned cv_ldo = (unsigned)(((tid >> 4) * 2 * 2048 + (tid & 15) * 4) * 4), cv_sto = (unsigned)((tid >> 3) * 2048 + 8 * (tid & 7));
;     const int cv_lw = OFF_CV + (4 * (tid & 15)) * 68 + 2 * (tid >> 4), cv_lr = OFF_CV + (tid >> 3) * 68 + 8 * (tid & 7);
;     f32x4 cvA = f32x4{}, cvB = f32x4{}; unsigned cvr0 = 0, cvr1 = 0;
.LBB4_722:
	s_lshl_b32 s26, s58, 8
	s_and_b32 s26, s26, 0x1f00
	s_add_u32 s80, s12, s26
	s_addc_u32 s81, s13, 0
	s_add_u32 s82, s80, 0x2000
	s_addc_u32 s83, s81, 0
	v_mov_b32_e32 v252, v209
	global_load_dwordx4 v[160:163], v252, s[80:81] nt
	global_load_dwordx4 v[164:167], v252, s[82:83] nt
.LBB4_723:
	v_exp_f32_e32 v186, v128
	v_exp_f32_e32 v230, v129
	v_exp_f32_e32 v231, v130
	v_exp_f32_e32 v232, v131
	v_exp_f32_e32 v233, v132
	v_exp_f32_e32 v234, v133
	v_exp_f32_e32 v235, v134
	v_exp_f32_e32 v236, v135
	v_exp_f32_e32 v237, v136
	v_exp_f32_e32 v238, v137
	v_exp_f32_e32 v239, v138
	v_exp_f32_e32 v240, v139
	v_exp_f32_e32 v241, v140
	v_exp_f32_e32 v242, v141
	v_exp_f32_e32 v243, v142
	v_exp_f32_e32 v244, v143
	v_add_u32_e32 v101, s78, v205
	v_add_u32_e32 v102, s78, v206
	v_add_u32_e32 v103, s78, v207
	ds_read_b128 v[172:175], v101 offset:49152
	ds_read_b128 v[176:179], v101 offset:53248
	ds_read_b128 v[214:217], v102 offset:49152
	ds_read_b128 v[218:221], v102 offset:53248
	ds_read_b128 v[222:225], v103 offset:49152
	ds_read_b128 v[226:229], v103 offset:53248
	v_exp_f32_e32 v112, v112
	v_exp_f32_e32 v113, v113
	v_exp_f32_e32 v114, v114
	s_waitcnt lgkmcnt(7)
	v_mfma_f32_32x32x16_bf16 v[128:143], v[96:99], v[156:159], v[80:95]
	v_exp_f32_e32 v115, v115
	v_exp_f32_e32 v116, v116
	v_exp_f32_e32 v117, v117
	v_exp_f32_e32 v118, v118
	v_exp_f32_e32 v119, v119
	s_waitcnt lgkmcnt(6)
	v_mfma_f32_32x32x16_bf16 v[96:111], v[168:171], v[156:159], v[80:95]
	v_exp_f32_e32 v168, v120
	v_add_f32_e32 v120, 0, v186
	v_add_f32_e32 v120, v230, v120
	v_add_f32_e32 v120, v231, v120
	v_add_f32_e32 v120, v232, v120
	v_add_f32_e32 v120, v233, v120
	v_add_f32_e32 v120, v234, v120
	v_add_f32_e32 v120, v235, v120
	v_add_f32_e32 v120, v236, v120
	v_add_f32_e32 v120, v237, v120
	v_add_f32_e32 v120, v238, v120
	s_waitcnt lgkmcnt(5)
	v_mfma_f32_32x32x16_bf16 v[128:143], v[172:175], v[152:155], v[128:143]
	v_add_f32_e32 v120, v239, v120
	v_add_f32_e32 v120, v240, v120
	v_add_f32_e32 v120, v241, v120
	v_add_f32_e32 v120, v242, v120
	v_add_f32_e32 v120, v243, v120
	v_add_f32_e32 v120, v244, v120
	v_add_f32_e32 v120, v112, v120
	s_waitcnt lgkmcnt(4)
	v_mfma_f32_32x32x16_bf16 v[96:111], v[176:179], v[152:155], v[96:111]
	v_add_f32_e32 v120, v113, v120
	v_add_f32_e32 v120, v114, v120
	v_add_f32_e32 v120, v115, v120
	v_add_f32_e32 v120, v116, v120
	v_exp_f32_e32 v169, v121
	v_add_f32_e32 v120, v117, v120
	v_exp_f32_e32 v170, v122
	s_waitcnt lgkmcnt(3)
	v_mfma_f32_32x32x16_bf16 v[128:143], v[214:217], v[148:151], v[128:143]
	v_add_f32_e32 v120, v118, v120
	v_exp_f32_e32 v171, v123
	v_add_f32_e32 v120, v119, v120
	v_exp_f32_e32 v172, v124
	v_add_f32_e32 v120, v168, v120
	v_exp_f32_e32 v173, v125
	v_add_f32_e32 v120, v169, v120
	s_waitcnt lgkmcnt(2)
	v_mfma_f32_32x32x16_bf16 v[96:111], v[218:221], v[148:151], v[96:111]
	v_exp_f32_e32 v174, v126
	v_add_f32_e32 v120, v170, v120
	v_exp_f32_e32 v175, v127
	v_add_f32_e32 v120, v171, v120
	v_add_f32_e32 v120, v172, v120
	v_add_f32_e32 v120, v173, v120
	v_add_f32_e32 v120, v174, v120
	s_waitcnt lgkmcnt(1)
	v_mfma_f32_32x32x16_bf16 v[128:143], v[222:225], v[144:147], v[128:143]
	v_add_f32_e32 v213, v175, v120
	v_mov_b32_e32 v214, v213
	v_cvt_pk_bf16_f32 v120, v186, v230
	v_cvt_pk_bf16_f32 v121, v231, v232
	v_cvt_pk_bf16_f32 v122, v233, v234
	v_cvt_pk_bf16_f32 v123, v235, v236
	v_cvt_pk_bf16_f32 v124, v237, v238
	s_waitcnt lgkmcnt(0)
	v_mfma_f32_32x32x16_bf16 v[96:111], v[226:229], v[144:147], v[96:111]
	v_cvt_pk_bf16_f32 v125, v239, v240
	v_cvt_pk_bf16_f32 v126, v241, v242
	v_cvt_pk_bf16_f32 v127, v243, v244
	v_cvt_pk_bf16_f32 v112, v112, v113
	v_cvt_pk_bf16_f32 v113, v114, v115
	v_cvt_pk_bf16_f32 v114, v116, v117
	v_cvt_pk_bf16_f32 v115, v118, v119
	v_cvt_pk_bf16_f32 v116, v168, v169
	v_cvt_pk_bf16_f32 v117, v170, v171
	v_cvt_pk_bf16_f32 v118, v172, v173
	v_cvt_pk_bf16_f32 v119, v174, v175
	v_permlane32_swap_b32_e32 v213, v214
	v_permlane32_swap_b32_e32 v120, v122
	v_permlane32_swap_b32_e32 v121, v123
	v_permlane32_swap_b32_e32 v124, v126
	v_permlane32_swap_b32_e32 v125, v127
	v_permlane32_swap_b32_e32 v112, v114
	v_permlane32_swap_b32_e32 v113, v115
	v_permlane32_swap_b32_e32 v116, v118
	v_permlane32_swap_b32_e32 v117, v119
	s_add_u32 s78, s74, 0x2380c000
	s_addc_u32 s79, s75, 0
	s_add_u32 s74, s74, 0x2380e000
	s_addc_u32 s75, s75, 0
	s_add_u32 s76, s76, 0x21806000
	s_addc_u32 s77, s77, 0
	v_mov_b32_e32 v168, v198
	v_mov_b32_e32 v169, v197
	global_load_dwordx4 v[176:179], v169, s[78:79]
	global_load_dwordx4 v[172:175], v169, s[74:75]
	s_nop 0
	global_load_dwordx4 v[168:171], v168, s[76:77]
	s_and_b64 vcc, exec, s[2:3]
	s_cbranch_vccnz .LBB4_725
	s_mov_b64 s[2:3], s[8:9]
	v_mov_b32_e32 v186, v189
	global_store_dwordx2 v186, v[184:185], s[2:3] nt

; #define AT_SWRITE(b, i) do { *(bf16x8*)(V_lds + (b) * SHM_V + vst0) = sr_[i].vs0; *(bf16x8*)(V_lds + (b) * SHM_V + vst1) = sr_[i].vs1; *(bf16x8*)(K_lds + (b) * SHM_K + kst) = sr_[i].ks0; } while (0)
; DI void qkt(f32x16& p0, f32x16& p1, const char* Ks, const bf16x8* qr, const f32x16& negm, int r32, int hi) {
; #pragma unroll
;     for (int d0 = 0; d0 < 4; ++d0) { const int cb = (d0 * 16 + hi * 8) * 2;
;         const bf16x8 b0 = *reinterpret_cast<const bf16x8*>(Ks + AT_KSWZ(r32, cb));
;         const bf16x8 b1 = *reinterpret_cast<const bf16x8*>(Ks + AT_KSWZ(32 + r32, cb));
;         p0 = __builtin_amdgcn_mfma_f32_32x32x16_bf16(b0, qr[d0], d0 == 0 ? negm : p0, 0, 0, 0);
;         p1 = __builtin_amdgcn_mfma_f32_32x32x16_bf16(b1, qr[d0], d0 == 0 ? negm : p1, 0, 0, 0); }
; }
; DI void attn_pass(const Frame& F, CvRide& cv, const bf16_t* __restrict__ Qb, const bf16_t* __restrict__ Kh, const bf16_t* __restrict__ Vh, char* lds, f32x16 (&o)[4], float& l_out, const int wave_s) {
;     ...
;     f32x16 pA0, pA1, pB0, pB1; float alA, alB; bf16x8 pa0, pa1, pa2, pa3; constexpr int NT = S / 64;
;     constexpr int SE = 0;
;     {
;         bf16x8 v10 = *reinterpret_cast<const bf16x8*>(&Vh[(size_t)(64 + sr) * 128 + sc]), v11 = *reinterpret_cast<const bf16x8*>(&Vh[(size_t)(96 + sr) * 128 + sc]);
;         bf16x8 k10 = *reinterpret_cast<const bf16x8*>(&Kh[(size_t)(64 + kr) * 64 + (tid & 7) * 8]);
;         AT_SLOAD(SE, 0); asm volatile("s_waitcnt vmcnt(0)" ::: "memory");
;         __syncthreads();
;         AT_SWRITE(0, SE);
;         *(bf16x8*)(V_lds + SHM_V + vst0) = v10; *(bf16x8*)(V_lds + SHM_V + vst1) = v11; *(bf16x8*)(K_lds + SHM_K + kst) = k10;
;         __syncthreads();
;     }
;     qkt(pA0, pA1, K_lds, qr, negm, r32, hi); partialSM(pA0, pA1, m_ref, negm, alA);
;     int s_prev = 0, s_cur = 1, s_next = 2;
.LBB4_765:
	s_lshl_b32 s92, s29, 13
	v_add_u32_e32 v68, s92, v207
	ds_read_b128 v[64:67], v68 offset:49152
	ds_read_b128 v[68:71], v68 offset:53248
	s_cmp_lg_u32 s20, 0
	s_mov_b32 s30, s29
	s_cselect_b64 s[2:3], -1, 0
	s_cmp_eq_u32 s20, 0
	s_mov_b32 s29, s22
	s_cbranch_scc1 .LBB4_767
	s_andn2_b32 s20, 1, s58
	s_mulk_i32 s20, 0x1100
	v_add_u32_e32 v252, s20, v194
	ds_read2_b32 v[184:185], v252 offset1:1

; DI void finishSM(f32x16& p0, f32x16& p1, float alpha, float& l_reg, bf16x8& pa0, bf16x8& pa1, bf16x8& pa2, bf16x8& pa3) {
; #pragma unroll
;     for (int r = 0; r < 16; ++r) p1[r] = __builtin_amdgcn_exp2f(p1[r]);
;     float ps = 0;
; #pragma unroll
;     for (int r = 0; r < 16; ++r) ps += p0[r];
; #pragma unroll
;     for (int r = 0; r < 16; ++r) ps += p1[r];
;     { auto rr = __builtin_amdgcn_permlane32_swap(__float_as_uint(ps), __float_as_uint(ps), false, false); ps = __uint_as_float(rr[0]) + __uint_as_float(rr[1]); }
;     l_reg = l_reg * alpha + ps;
;     ...
;     AT_PK4(p0, 0, pa0); AT_PK4(p0, 8, pa1); AT_PK4(p1, 0, pa2); AT_PK4(p1, 8, pa3);
;     ...
; }
; DI void qkt(f32x16& p0, f32x16& p1, const char* Ks, const bf16x8* qr, const f32x16& negm, int r32, int hi) {
; #pragma unroll
;     for (int d0 = 0; d0 < 4; ++d0) { const int cb = (d0 * 16 + hi * 8) * 2;
;         const bf16x8 b0 = *reinterpret_cast<const bf16x8*>(Ks + AT_KSWZ(r32, cb));
;         const bf16x8 b1 = *reinterpret_cast<const bf16x8*>(Ks + AT_KSWZ(32 + r32, cb));
;         p0 = __builtin_amdgcn_mfma_f32_32x32x16_bf16(b0, qr[d0], d0 == 0 ? negm : p0, 0, 0, 0);
;         p1 = __builtin_amdgcn_mfma_f32_32x32x16_bf16(b1, qr[d0], d0 == 0 ? negm : p1, 0, 0, 0); }
; }
; DI void attn_pass(const Frame& F, CvRide& cv, const bf16_t* __restrict__ Qb, const bf16_t* __restrict__ Kh, const bf16_t* __restrict__ Vh, char* lds, f32x16 (&o)[4], float& l_out, const int wave_s) {
;     ...
;     const unsigned cv_ldo = (unsigned)(((tid >> 4) * 2 * 2048 + (tid & 15) * 4) * 4), cv_sto = (unsigned)((tid >> 3) * 2048 + 8 * (tid & 7));
;     const int cv_lw = OFF_CV + (4 * (tid & 15)) * 68 + 2 * (tid >> 4), cv_lr = OFF_CV + (tid >> 3) * 68 + 8 * (tid & 7);
;     f32x4 cvA = f32x4{}, cvB = f32x4{}; unsigned cvr0 = 0, cvr1 = 0;
.LBB4_774:
	s_lshl_b32 s20, s58, 8
	s_and_b32 s20, s20, 0x1f00
	s_add_u32 s24, s12, s20
	s_addc_u32 s25, s13, 0
	s_add_u32 s34, s24, 0x2000
	s_addc_u32 s35, s25, 0
	v_mov_b32_e32 v252, v213
	global_load_dwordx4 v[160:163], v252, s[24:25] nt
	global_load_dwordx4 v[164:167], v252, s[34:35] nt
.LBB4_775:
	s_lshl_b32 s20, s30, 13
	s_add_i32 s20, s20, 0
	v_add_u32_e32 v72, s20, v208
	v_add_u32_e32 v112, s20, v209
	v_add_u32_e32 v180, s20, v210
	s_waitcnt lgkmcnt(1)
	v_mfma_f32_32x32x16_bf16 v[128:143], v[64:67], v[156:159], v[80:95]
	ds_read_b128 v[64:67], v72 offset:49152
	ds_read_b128 v[72:75], v72 offset:53248
	ds_read_b128 v[76:79], v112 offset:49152
	ds_read_b128 v[224:227], v112 offset:53248
	v_exp_f32_e32 v182, v97
	v_exp_f32_e32 v217, v98
	v_exp_f32_e32 v218, v99
	v_exp_f32_e32 v223, v100
	v_exp_f32_e32 v232, v101
	s_waitcnt lgkmcnt(4)
	v_mfma_f32_32x32x16_bf16 v[112:127], v[68:71], v[156:159], v[80:95]
	ds_read_b128 v[68:71], v180 offset:49152
	ds_read_b128 v[228:231], v180 offset:53248
	v_exp_f32_e32 v180, v96
	v_cvt_pk_bf16_f32 v96, v220, v222
	v_cvt_pk_bf16_f32 v97, v179, v221
	v_cvt_pk_bf16_f32 v98, v177, v219
	v_cvt_pk_bf16_f32 v99, v176, v178
	s_waitcnt lgkmcnt(4)
	v_mfma_f32_32x32x16_bf16 v[112:127], v[72:75], v[152:155], v[112:127]
	v_add_f32_e32 v75, 0, v220
	v_add_f32_e32 v75, v222, v75
	v_add_f32_e32 v75, v179, v75
	v_add_f32_e32 v75, v221, v75
	v_add_f32_e32 v75, v177, v75
	v_add_f32_e32 v75, v219, v75
	v_add_f32_e32 v75, v176, v75
	v_mfma_f32_32x32x16_bf16 v[128:143], v[64:67], v[152:155], v[128:143]
	v_add_f32_e32 v75, v178, v75
	v_add_f32_e32 v75, v173, v75
	v_add_f32_e32 v75, v175, v75
	v_add_f32_e32 v75, v171, v75
	v_add_f32_e32 v75, v174, v75
	v_add_f32_e32 v75, v169, v75
	v_add_f32_e32 v75, v172, v75
	s_waitcnt lgkmcnt(3)
	v_mfma_f32_32x32x16_bf16 v[128:143], v[76:79], v[148:151], v[128:143]
	v_add_f32_e32 v75, v168, v75
	v_add_f32_e32 v75, v170, v75
	v_add_f32_e32 v75, v180, v75
	v_add_f32_e32 v75, v182, v75
	v_exp_f32_e32 v64, v102
	v_exp_f32_e32 v65, v103
	v_exp_f32_e32 v66, v104
	s_waitcnt lgkmcnt(2)
	v_mfma_f32_32x32x16_bf16 v[112:127], v[224:227], v[148:151], v[112:127]
	v_exp_f32_e32 v67, v105
	v_exp_f32_e32 v105, v106
	v_exp_f32_e32 v106, v107
	v_exp_f32_e32 v107, v108
	v_exp_f32_e32 v72, v109
	v_exp_f32_e32 v73, v110
	v_exp_f32_e32 v74, v111
	s_waitcnt lgkmcnt(1)
	v_mfma_f32_32x32x16_bf16 v[128:143], v[68:71], v[144:147], v[128:143]
	v_add_f32_e32 v68, v217, v75
	v_add_f32_e32 v68, v218, v68
	v_add_f32_e32 v68, v223, v68
	v_add_f32_e32 v68, v232, v68
	v_add_f32_e32 v68, v64, v68
	v_add_f32_e32 v68, v65, v68
	v_add_f32_e32 v68, v66, v68
	v_add_f32_e32 v68, v67, v68
	s_waitcnt lgkmcnt(0)
	v_mfma_f32_32x32x16_bf16 v[112:127], v[228:231], v[144:147], v[112:127]
	v_add_f32_e32 v68, v105, v68
	v_add_f32_e32 v68, v106, v68
	v_add_f32_e32 v68, v107, v68
	v_add_f32_e32 v68, v72, v68
	v_add_f32_e32 v68, v73, v68
	v_add_f32_e32 v215, v74, v68
	v_mov_b32_e32 v216, v215
	v_cvt_pk_bf16_f32 v108, v173, v175
	v_cvt_pk_bf16_f32 v109, v171, v174
	v_cvt_pk_bf16_f32 v110, v169, v172
	v_cvt_pk_bf16_f32 v111, v168, v170
	v_cvt_pk_bf16_f32 v100, v180, v182
	v_cvt_pk_bf16_f32 v101, v217, v218
	v_cvt_pk_bf16_f32 v102, v223, v232
	v_cvt_pk_bf16_f32 v103, v64, v65
	v_cvt_pk_bf16_f32 v104, v66, v67
	v_cvt_pk_bf16_f32 v105, v105, v106
	v_cvt_pk_bf16_f32 v106, v107, v72
	v_cvt_pk_bf16_f32 v107, v73, v74
	s_nop 1
	v_permlane32_swap_b32_e32 v215, v216
	v_permlane32_swap_b32_e32 v96, v98
	v_permlane32_swap_b32_e32 v97, v99
	v_permlane32_swap_b32_e32 v108, v110
	v_permlane32_swap_b32_e32 v109, v111
	v_permlane32_swap_b32_e32 v100, v102
	v_permlane32_swap_b32_e32 v101, v103
	v_permlane32_swap_b32_e32 v104, v106
	v_permlane32_swap_b32_e32 v105, v107
	s_add_u32 s34, s46, s16
	s_addc_u32 s35, s47, s17
	s_add_u32 s24, s34, 0x23808000
	s_addc_u32 s25, s35, 0
	s_add_u32 s66, s34, 0x2380a000
	s_addc_u32 s67, s35, 0
	s_add_u32 s37, s46, s18
	s_addc_u32 s64, s47, s19
	s_add_u32 s74, s37, 0x21884000
	s_addc_u32 s75, s64, 0
	v_mov_b32_e32 v64, v200
	v_mov_b32_e32 v65, v201
	global_load_dwordx4 v[176:179], v64, s[24:25]
	global_load_dwordx4 v[172:175], v64, s[66:67]
	global_load_dwordx4 v[168:171], v65, s[74:75]
	s_andn2_b64 vcc, exec, s[2:3]
	s_cbranch_vccnz .LBB4_777
	s_mov_b64 s[2:3], s[8:9]
	v_mov_b32_e32 v64, v193
	global_store_dwordx2 v64, v[184:185], s[2:3] nt

; #define AT_SBAR() __builtin_amdgcn_sched_barrier(0)
; template <int OFF> DI s16x4 tr_read(int vb) { s16x4 r; asm volatile("ds_read_b64_tr_b16 %0, %1 offset:%2" : "=&v"(r) : "v"(vb), "i"(OFF) : "memory"); return r; }
; template <int D0> DI void pv_one(f32x16& od, int vb, bf16x8 pa0, bf16x8 pa1, bf16x8 pa2, bf16x8 pa3) {
;     const s16x4 l0 = tr_read<v_rd_off(D0, 0, 0)>(vb), h0 = tr_read<v_rd_off(D0, 0, 1)>(vb), l1 = tr_read<v_rd_off(D0, 1, 0)>(vb), h1 = tr_read<v_rd_off(D0, 1, 1)>(vb);
;     const s16x4 l2 = tr_read<v_rd_off(D0, 2, 0)>(vb), h2 = tr_read<v_rd_off(D0, 2, 1)>(vb), l3 = tr_read<v_rd_off(D0, 3, 0)>(vb), h3 = tr_read<v_rd_off(D0, 3, 1)>(vb);
;     asm volatile("s_waitcnt lgkmcnt(0)" ::: "memory"); AT_SBAR();
;     ...
;     od = __builtin_amdgcn_mfma_f32_32x32x16_bf16(AT_PK(l0, h0), pa0, od, 0, 0, 0);
;     od = __builtin_amdgcn_mfma_f32_32x32x16_bf16(AT_PK(l1, h1), pa1, od, 0, 0, 0);
;     od = __builtin_amdgcn_mfma_f32_32x32x16_bf16(AT_PK(l2, h2), pa2, od, 0, 0, 0);
;     od = __builtin_amdgcn_mfma_f32_32x32x16_bf16(AT_PK(l3, h3), pa3, od, 0, 0, 0);
;     ...
; }
; DI void attn_pass(const Frame& F, CvRide& cv, const bf16_t* __restrict__ Qb, const bf16_t* __restrict__ Kh, const bf16_t* __restrict__ Vh, char* lds, f32x16 (&o)[4], float& l_out, const int wave_s) {
;     ...
;     const unsigned cv_ldo = (unsigned)(((tid >> 4) * 2 * 2048 + (tid & 15) * 4) * 4), cv_sto = (unsigned)((tid >> 3) * 2048 + 8 * (tid & 7));
;     const int cv_lw = OFF_CV + (4 * (tid & 15)) * 68 + 2 * (tid >> 4), cv_lr = OFF_CV + (tid >> 3) * 68 + 8 * (tid & 7);
;     f32x4 cvA = f32x4{}, cvB = f32x4{}; unsigned cvr0 = 0, cvr1 = 0;
.LBB4_779:
	ds_read_b64_tr_b16 v[218:219], v182 offset:0x600
	ds_read_b64_tr_b16 v[220:221], v182 offset:0xe00
	ds_read_b64_tr_b16 v[222:223], v182 offset:0x1600
	ds_read_b64_tr_b16 v[224:225], v182 offset:0x1e00
	ds_read_b64_tr_b16 v[226:227], v182 offset:0x2600
	ds_read_b64_tr_b16 v[228:229], v182 offset:0x2e00
	ds_read_b64_tr_b16 v[230:231], v182 offset:0x3600
	ds_read_b64_tr_b16 v[232:233], v182 offset:0x3e00
	s_waitcnt lgkmcnt(0)
	s_nop 0
	v_mfma_f32_32x32x16_bf16 v[0:15], v[218:221], v[96:99], v[0:15]
	s_lshl_b32 s2, s15, 14
	s_add_i32 s2, s2, 0
	s_lshl_b32 s3, s15, 13
	v_add_u32_e32 v96, s2, v203
	s_sub_i32 s65, s2, s3
	s_waitcnt vmcnt(0)
	v_add_u32_e32 v97, s2, v204
	v_mfma_f32_32x32x16_bf16 v[0:15], v[222:225], v[108:111], v[0:15]
	ds_write_b128 v96, v[176:179]
	v_add_u32_e32 v96, s65, v205
	ds_write_b128 v97, v[172:175]
	ds_write_b128 v96, v[168:171] offset:49152
	s_andn2_b64 s[2:3], exec, s[22:23]
	s_andn2_b64 vcc, exec, s[22:23]
	v_mfma_f32_32x32x16_bf16 v[0:15], v[226:229], v[100:103], v[0:15]
	v_mfma_f32_32x32x16_bf16 v[0:15], v[230:233], v[104:107], v[0:15]
	s_cbranch_vccnz .LBB4_784
	v_mul_f32_e32 v97, 0x44000000, v160
	v_mul_f32_e32 v98, 0x44000000, v164
	v_med3_f32 v97, v97, s28, v214
	v_med3_f32 v98, v98, s28, v214
	v_cvt_pk_fp8_f32 v99, v97, v98
	v_mul_f32_e32 v97, 0x44000000, v161
	v_mul_f32_e32 v98, 0x44000000, v165
	v_med3_f32 v97, v97, s28, v214
	v_med3_f32 v98, v98, s28, v214
	v_cvt_pk_fp8_f32 v100, v97, v98
	v_mul_f32_e32 v97, 0x44000000, v162
	v_mul_f32_e32 v98, 0x44000000, v166
	v_med3_f32 v97, v97, s28, v214
	v_med3_f32 v98, v98, s28, v214
	s_bitcmp1_b32 s58, 0
	v_cvt_pk_fp8_f32 v101, v97, v98
	v_mul_f32_e32 v97, 0x44000000, v163
	v_mul_f32_e32 v98, 0x44000000, v167
	s_cselect_b32 s8, 0x1100, 0
	v_med3_f32 v97, v97, s28, v214
	v_med3_f32 v98, v98, s28, v214
	v_cmp_eq_u32_e32 vcc, 0, v181
	v_add_u32_e32 v96, s8, v195
	v_cvt_pk_fp8_f32 v102, v97, v98
	s_and_b64 vcc, exec, vcc
	s_and_b32 s22, s58, 31
	ds_write_b16 v96, v99
	ds_write_b16 v96, v100 offset:68
	ds_write_b16 v96, v101 offset:136
	ds_write_b16 v96, v102 offset:204
	s_cbranch_vccnz .LBB4_808
	s_lshl_b32 s8, s22, 7
	s_lshl_b32 s9, s58, 6
	s_and_b32 s8, s8, 0xf00
	s_and_b32 s9, s9, 64
	s_or_b32 s20, s8, s9
	s_cbranch_execnz .LBB4_783

; #define AT_SWRITE(b, i) do { *(bf16x8*)(V_lds + (b) * SHM_V + vst0) = sr_[i].vs0; *(bf16x8*)(V_lds + (b) * SHM_V + vst1) = sr_[i].vs1; *(bf16x8*)(K_lds + (b) * SHM_K + kst) = sr_[i].ks0; } while (0)
; DI void attn_pass(const Frame& F, CvRide& cv, const bf16_t* __restrict__ Qb, const bf16_t* __restrict__ Kh, const bf16_t* __restrict__ Vh, char* lds, f32x16 (&o)[4], float& l_out, const int wave_s) {
;     ...
;     f32x16 pA0, pA1, pB0, pB1; float alA, alB; bf16x8 pa0, pa1, pa2, pa3; constexpr int NT = S / 64;
;     constexpr int SE = 0;
;     {
;         bf16x8 v10 = *reinterpret_cast<const bf16x8*>(&Vh[(size_t)(64 + sr) * 128 + sc]), v11 = *reinterpret_cast<const bf16x8*>(&Vh[(size_t)(96 + sr) * 128 + sc]);
;         bf16x8 k10 = *reinterpret_cast<const bf16x8*>(&Kh[(size_t)(64 + kr) * 64 + (tid & 7) * 8]);
;         AT_SLOAD(SE, 0); asm volatile("s_waitcnt vmcnt(0)" ::: "memory");
;         __syncthreads();
;         AT_SWRITE(0, SE);
;         *(bf16x8*)(V_lds + SHM_V + vst0) = v10; *(bf16x8*)(V_lds + SHM_V + vst1) = v11; *(bf16x8*)(K_lds + SHM_K + kst) = k10;
;         __syncthreads();
;     }
;     qkt(pA0, pA1, K_lds, qr, negm, r32, hi); partialSM(pA0, pA1, m_ref, negm, alA);
;     int s_prev = 0, s_cur = 1, s_next = 2;
.LBB4_786:
	s_and_b64 vcc, exec, s[2:3]
	s_waitcnt lgkmcnt(0)
	s_barrier
	v_add_u32_e32 v100, s65, v207
	ds_read_b128 v[96:99], v100 offset:49152
	ds_read_b128 v[168:171], v100 offset:53248
	s_cbranch_vccnz .LBB4_788
	s_andn2_b32 s20, 1, s58
	s_mulk_i32 s20, 0x1100
	v_add_u32_e32 v252, s20, v194
	ds_read2_b32 v[184:185], v252 offset1:1

; DI void finishSM(f32x16& p0, f32x16& p1, float alpha, float& l_reg, bf16x8& pa0, bf16x8& pa1, bf16x8& pa2, bf16x8& pa3) {
; #pragma unroll
;     for (int r = 0; r < 16; ++r) p1[r] = __builtin_amdgcn_exp2f(p1[r]);
;     float ps = 0;
; #pragma unroll
;     for (int r = 0; r < 16; ++r) ps += p0[r];
; #pragma unroll
;     for (int r = 0; r < 16; ++r) ps += p1[r];
;     { auto rr = __builtin_amdgcn_permlane32_swap(__float_as_uint(ps), __float_as_uint(ps), false, false); ps = __uint_as_float(rr[0]) + __uint_as_float(rr[1]); }
;     l_reg = l_reg * alpha + ps;
;     ...
;     AT_PK4(p0, 0, pa0); AT_PK4(p0, 8, pa1); AT_PK4(p1, 0, pa2); AT_PK4(p1, 8, pa3);
;     ...
; }
; DI void qkt(f32x16& p0, f32x16& p1, const char* Ks, const bf16x8* qr, const f32x16& negm, int r32, int hi) {
; #pragma unroll
;     for (int d0 = 0; d0 < 4; ++d0) { const int cb = (d0 * 16 + hi * 8) * 2;
;         const bf16x8 b0 = *reinterpret_cast<const bf16x8*>(Ks + AT_KSWZ(r32, cb));
;         const bf16x8 b1 = *reinterpret_cast<const bf16x8*>(Ks + AT_KSWZ(32 + r32, cb));
;         p0 = __builtin_amdgcn_mfma_f32_32x32x16_bf16(b0, qr[d0], d0 == 0 ? negm : p0, 0, 0, 0);
;         p1 = __builtin_amdgcn_mfma_f32_32x32x16_bf16(b1, qr[d0], d0 == 0 ? negm : p1, 0, 0, 0); }
; }
; DI void attn_pass(const Frame& F, CvRide& cv, const bf16_t* __restrict__ Qb, const bf16_t* __restrict__ Kh, const bf16_t* __restrict__ Vh, char* lds, f32x16 (&o)[4], float& l_out, const int wave_s) {
;     ...
;     const unsigned cv_ldo = (unsigned)(((tid >> 4) * 2 * 2048 + (tid & 15) * 4) * 4), cv_sto = (unsigned)((tid >> 3) * 2048 + 8 * (tid & 7));
;     const int cv_lw = OFF_CV + (4 * (tid & 15)) * 68 + 2 * (tid >> 4), cv_lr = OFF_CV + (tid >> 3) * 68 + 8 * (tid & 7);
;     f32x4 cvA = f32x4{}, cvB = f32x4{}; unsigned cvr0 = 0, cvr1 = 0;
.LBB4_795:
	s_lshl_b32 s20, s58, 8
	s_and_b32 s20, s20, 0x1f00
	s_add_u32 s24, s12, s20
	s_addc_u32 s25, s13, 0
	s_add_u32 s66, s24, 0x2000
	s_addc_u32 s67, s25, 0
	v_mov_b32_e32 v252, v213
	global_load_dwordx4 v[160:163], v252, s[24:25] nt
	global_load_dwordx4 v[164:167], v252, s[66:67] nt
.LBB4_796:
	v_exp_f32_e32 v182, v128
	v_exp_f32_e32 v234, v129
	v_exp_f32_e32 v235, v130
	v_exp_f32_e32 v236, v131
	v_exp_f32_e32 v237, v132
	v_exp_f32_e32 v238, v133
	v_exp_f32_e32 v239, v134
	v_exp_f32_e32 v240, v135
	v_exp_f32_e32 v241, v136
	v_exp_f32_e32 v242, v137
	v_exp_f32_e32 v243, v138
	v_exp_f32_e32 v244, v139
	v_exp_f32_e32 v245, v140
	v_exp_f32_e32 v246, v141
	v_exp_f32_e32 v247, v142
	v_exp_f32_e32 v248, v143
	v_add_u32_e32 v101, s65, v208
	v_add_u32_e32 v102, s65, v209
	v_add_u32_e32 v103, s65, v210
	ds_read_b128 v[172:175], v101 offset:49152
	ds_read_b128 v[176:179], v101 offset:53248
	ds_read_b128 v[218:221], v102 offset:49152
	ds_read_b128 v[222:225], v102 offset:53248
	ds_read_b128 v[226:229], v103 offset:49152
	ds_read_b128 v[230:233], v103 offset:53248
	v_exp_f32_e32 v112, v112
	v_exp_f32_e32 v113, v113
	v_exp_f32_e32 v114, v114
	s_waitcnt lgkmcnt(7)
	v_mfma_f32_32x32x16_bf16 v[128:143], v[96:99], v[156:159], v[80:95]
	v_exp_f32_e32 v115, v115
	v_exp_f32_e32 v116, v116
	v_exp_f32_e32 v117, v117
	v_exp_f32_e32 v118, v118
	v_exp_f32_e32 v119, v119
	s_waitcnt lgkmcnt(6)
	v_mfma_f32_32x32x16_bf16 v[96:111], v[168:171], v[156:159], v[80:95]
	v_exp_f32_e32 v168, v120
	v_add_f32_e32 v120, 0, v182
	v_add_f32_e32 v120, v234, v120
	v_add_f32_e32 v120, v235, v120
	v_add_f32_e32 v120, v236, v120
	v_add_f32_e32 v120, v237, v120
	v_add_f32_e32 v120, v238, v120
	v_add_f32_e32 v120, v239, v120
	v_add_f32_e32 v120, v240, v120
	v_add_f32_e32 v120, v241, v120
	v_add_f32_e32 v120, v242, v120
	s_waitcnt lgkmcnt(5)
	v_mfma_f32_32x32x16_bf16 v[128:143], v[172:175], v[152:155], v[128:143]
	v_add_f32_e32 v120, v243, v120
	v_add_f32_e32 v120, v244, v120
	v_add_f32_e32 v120, v245, v120
	v_add_f32_e32 v120, v246, v120
	v_add_f32_e32 v120, v247, v120
	v_add_f32_e32 v120, v248, v120
	v_add_f32_e32 v120, v112, v120
	s_waitcnt lgkmcnt(4)
	v_mfma_f32_32x32x16_bf16 v[96:111], v[176:179], v[152:155], v[96:111]
	v_add_f32_e32 v120, v113, v120
	v_add_f32_e32 v120, v114, v120
	v_add_f32_e32 v120, v115, v120
	v_add_f32_e32 v120, v116, v120
	v_exp_f32_e32 v169, v121
	v_add_f32_e32 v120, v117, v120
	v_exp_f32_e32 v170, v122
	s_waitcnt lgkmcnt(3)
	v_mfma_f32_32x32x16_bf16 v[128:143], v[218:221], v[148:151], v[128:143]
	v_add_f32_e32 v120, v118, v120
	v_exp_f32_e32 v171, v123
	v_add_f32_e32 v120, v119, v120
	v_exp_f32_e32 v172, v124
	v_add_f32_e32 v120, v168, v120
	v_exp_f32_e32 v173, v125
	v_add_f32_e32 v120, v169, v120
	s_waitcnt lgkmcnt(2)
	v_mfma_f32_32x32x16_bf16 v[96:111], v[222:225], v[148:151], v[96:111]
	v_exp_f32_e32 v174, v126
	v_add_f32_e32 v120, v170, v120
	v_exp_f32_e32 v175, v127
	v_add_f32_e32 v120, v171, v120
	v_add_f32_e32 v120, v172, v120
	v_add_f32_e32 v120, v173, v120
	v_add_f32_e32 v120, v174, v120
	s_waitcnt lgkmcnt(1)
	v_mfma_f32_32x32x16_bf16 v[128:143], v[226:229], v[144:147], v[128:143]
	v_add_f32_e32 v217, v175, v120
	v_mov_b32_e32 v218, v217
	v_cvt_pk_bf16_f32 v120, v182, v234
	v_cvt_pk_bf16_f32 v121, v235, v236
	v_cvt_pk_bf16_f32 v122, v237, v238
	v_cvt_pk_bf16_f32 v123, v239, v240
	v_cvt_pk_bf16_f32 v124, v241, v242
	s_waitcnt lgkmcnt(0)
	v_mfma_f32_32x32x16_bf16 v[96:111], v[230:233], v[144:147], v[96:111]
	v_cvt_pk_bf16_f32 v125, v243, v244
	v_cvt_pk_bf16_f32 v126, v245, v246
	v_cvt_pk_bf16_f32 v127, v247, v248
	v_cvt_pk_bf16_f32 v112, v112, v113
	v_cvt_pk_bf16_f32 v113, v114, v115
	v_cvt_pk_bf16_f32 v114, v116, v117
	v_cvt_pk_bf16_f32 v115, v118, v119
	v_cvt_pk_bf16_f32 v116, v168, v169
	v_cvt_pk_bf16_f32 v117, v170, v171
	v_cvt_pk_bf16_f32 v118, v172, v173
	v_cvt_pk_bf16_f32 v119, v174, v175
	v_permlane32_swap_b32_e32 v217, v218
	v_permlane32_swap_b32_e32 v120, v122
	v_permlane32_swap_b32_e32 v121, v123
	v_permlane32_swap_b32_e32 v124, v126
	v_permlane32_swap_b32_e32 v125, v127
	v_permlane32_swap_b32_e32 v112, v114
	v_permlane32_swap_b32_e32 v113, v115
	v_permlane32_swap_b32_e32 v116, v118
	v_permlane32_swap_b32_e32 v117, v119
	s_add_u32 s24, s34, 0x2380c000
	s_addc_u32 s25, s35, 0
	s_add_u32 s34, s34, 0x2380e000
	s_addc_u32 s35, s35, 0
	s_add_u32 s66, s37, 0x21886000
	s_addc_u32 s67, s64, 0
	v_mov_b32_e32 v168, v200
	v_mov_b32_e32 v169, v201
	global_load_dwordx4 v[176:179], v168, s[24:25]
	global_load_dwordx4 v[172:175], v168, s[34:35]
	s_nop 0
	global_load_dwordx4 v[168:171], v169, s[66:67]
	s_and_b64 vcc, exec, s[2:3]
	s_cbranch_vccnz .LBB4_798
	v_mov_b32_e32 v182, v193
	s_mov_b64 s[2:3], s[8:9]
	global_store_dwordx2 v182, v[184:185], s[2:3] nt

; #define AT_SWRITE(b, i) do { *(bf16x8*)(V_lds + (b) * SHM_V + vst0) = sr_[i].vs0; *(bf16x8*)(V_lds + (b) * SHM_V + vst1) = sr_[i].vs1; *(bf16x8*)(K_lds + (b) * SHM_K + kst) = sr_[i].ks0; } while (0)
; DI void qkt(f32x16& p0, f32x16& p1, const char* Ks, const bf16x8* qr, const f32x16& negm, int r32, int hi) {
; #pragma unroll
;     for (int d0 = 0; d0 < 4; ++d0) { const int cb = (d0 * 16 + hi * 8) * 2;
;         const bf16x8 b0 = *reinterpret_cast<const bf16x8*>(Ks + AT_KSWZ(r32, cb));
;         const bf16x8 b1 = *reinterpret_cast<const bf16x8*>(Ks + AT_KSWZ(32 + r32, cb));
;         p0 = __builtin_amdgcn_mfma_f32_32x32x16_bf16(b0, qr[d0], d0 == 0 ? negm : p0, 0, 0, 0);
;         p1 = __builtin_amdgcn_mfma_f32_32x32x16_bf16(b1, qr[d0], d0 == 0 ? negm : p1, 0, 0, 0); }
; }
; DI void attn_pass(const Frame& F, CvRide& cv, const bf16_t* __restrict__ Qb, const bf16_t* __restrict__ Kh, const bf16_t* __restrict__ Vh, char* lds, f32x16 (&o)[4], float& l_out, const int wave_s) {
;     ...
;     f32x16 pA0, pA1, pB0, pB1; float alA, alB; bf16x8 pa0, pa1, pa2, pa3; constexpr int NT = S / 64;
;     constexpr int SE = 0;
;     {
;         bf16x8 v10 = *reinterpret_cast<const bf16x8*>(&Vh[(size_t)(64 + sr) * 128 + sc]), v11 = *reinterpret_cast<const bf16x8*>(&Vh[(size_t)(96 + sr) * 128 + sc]);
;         bf16x8 k10 = *reinterpret_cast<const bf16x8*>(&Kh[(size_t)(64 + kr) * 64 + (tid & 7) * 8]);
;         AT_SLOAD(SE, 0); asm volatile("s_waitcnt vmcnt(0)" ::: "memory");
;         __syncthreads();
;         AT_SWRITE(0, SE);
;         *(bf16x8*)(V_lds + SHM_V + vst0) = v10; *(bf16x8*)(V_lds + SHM_V + vst1) = v11; *(bf16x8*)(K_lds + SHM_K + kst) = k10;
;         __syncthreads();
;     }
;     qkt(pA0, pA1, K_lds, qr, negm, r32, hi); partialSM(pA0, pA1, m_ref, negm, alA);
;     int s_prev = 0, s_cur = 1, s_next = 2;
.LBB4_839:
	s_lshl_b32 s92, s63, 13
	v_add_u32_e32 v68, s92, v203
	ds_read_b128 v[64:67], v68 offset:49152
	ds_read_b128 v[68:71], v68 offset:53248
	s_cmp_lg_u32 s26, 0
	s_mov_b32 s64, s63
	s_cselect_b64 s[2:3], -1, 0
	s_cmp_eq_u32 s26, 0
	s_mov_b32 s63, s30
	s_cbranch_scc1 .LBB4_841
	s_andn2_b32 s26, 1, s58
	s_mulk_i32 s26, 0x1100
	v_add_u32_e32 v252, s26, v189
	ds_read2_b32 v[184:185], v252 offset1:1

; DI void finishSM(f32x16& p0, f32x16& p1, float alpha, float& l_reg, bf16x8& pa0, bf16x8& pa1, bf16x8& pa2, bf16x8& pa3) {
; #pragma unroll
;     for (int r = 0; r < 16; ++r) p1[r] = __builtin_amdgcn_exp2f(p1[r]);
;     float ps = 0;
; #pragma unroll
;     for (int r = 0; r < 16; ++r) ps += p0[r];
; #pragma unroll
;     for (int r = 0; r < 16; ++r) ps += p1[r];
;     { auto rr = __builtin_amdgcn_permlane32_swap(__float_as_uint(ps), __float_as_uint(ps), false, false); ps = __uint_as_float(rr[0]) + __uint_as_float(rr[1]); }
;     l_reg = l_reg * alpha + ps;
;     ...
;     AT_PK4(p0, 0, pa0); AT_PK4(p0, 8, pa1); AT_PK4(p1, 0, pa2); AT_PK4(p1, 8, pa3);
;     ...
; }
; DI void qkt(f32x16& p0, f32x16& p1, const char* Ks, const bf16x8* qr, const f32x16& negm, int r32, int hi) {
; #pragma unroll
;     for (int d0 = 0; d0 < 4; ++d0) { const int cb = (d0 * 16 + hi * 8) * 2;
;         const bf16x8 b0 = *reinterpret_cast<const bf16x8*>(Ks + AT_KSWZ(r32, cb));
;         const bf16x8 b1 = *reinterpret_cast<const bf16x8*>(Ks + AT_KSWZ(32 + r32, cb));
;         p0 = __builtin_amdgcn_mfma_f32_32x32x16_bf16(b0, qr[d0], d0 == 0 ? negm : p0, 0, 0, 0);
;         p1 = __builtin_amdgcn_mfma_f32_32x32x16_bf16(b1, qr[d0], d0 == 0 ? negm : p1, 0, 0, 0); }
; }
; DI void attn_pass(const Frame& F, CvRide& cv, const bf16_t* __restrict__ Qb, const bf16_t* __restrict__ Kh, const bf16_t* __restrict__ Vh, char* lds, f32x16 (&o)[4], float& l_out, const int wave_s) {
;     ...
;     const unsigned cv_ldo = (unsigned)(((tid >> 4) * 2 * 2048 + (tid & 15) * 4) * 4), cv_sto = (unsigned)((tid >> 3) * 2048 + 8 * (tid & 7));
;     const int cv_lw = OFF_CV + (4 * (tid & 15)) * 68 + 2 * (tid >> 4), cv_lr = OFF_CV + (tid >> 3) * 68 + 8 * (tid & 7);
;     f32x4 cvA = f32x4{}, cvB = f32x4{}; unsigned cvr0 = 0, cvr1 = 0;
.LBB4_848:
	s_lshl_b32 s26, s58, 8
	s_and_b32 s26, s26, 0x1f00
	s_add_u32 s34, s12, s26
	s_addc_u32 s35, s13, 0
	s_add_u32 s66, s34, 0x2000
	s_addc_u32 s67, s35, 0
	v_mov_b32_e32 v252, v209
	global_load_dwordx4 v[160:163], v252, s[34:35] nt
	global_load_dwordx4 v[164:167], v252, s[66:67] nt
.LBB4_849:
	s_lshl_b32 s26, s64, 13
	s_add_i32 s26, s26, 0
	v_add_u32_e32 v72, s26, v204
	v_add_u32_e32 v112, s26, v205
	v_add_u32_e32 v180, s26, v206
	s_waitcnt lgkmcnt(1)
	v_mfma_f32_32x32x16_bf16 v[128:143], v[64:67], v[156:159], v[80:95]
	ds_read_b128 v[64:67], v72 offset:49152
	ds_read_b128 v[72:75], v72 offset:53248
	ds_read_b128 v[76:79], v112 offset:49152
	ds_read_b128 v[220:223], v112 offset:53248
	v_exp_f32_e32 v182, v97
	v_exp_f32_e32 v213, v98
	v_exp_f32_e32 v214, v99
	v_exp_f32_e32 v219, v100
	v_exp_f32_e32 v228, v101
	s_waitcnt lgkmcnt(4)
	v_mfma_f32_32x32x16_bf16 v[112:127], v[68:71], v[156:159], v[80:95]
	ds_read_b128 v[68:71], v180 offset:49152
	ds_read_b128 v[224:227], v180 offset:53248
	v_exp_f32_e32 v180, v96
	v_cvt_pk_bf16_f32 v96, v216, v218
	v_cvt_pk_bf16_f32 v97, v179, v217
	v_cvt_pk_bf16_f32 v98, v177, v215
	v_cvt_pk_bf16_f32 v99, v176, v178
	s_waitcnt lgkmcnt(4)
	v_mfma_f32_32x32x16_bf16 v[112:127], v[72:75], v[152:155], v[112:127]
	v_add_f32_e32 v75, 0, v216
	v_add_f32_e32 v75, v218, v75
	v_add_f32_e32 v75, v179, v75
	v_add_f32_e32 v75, v217, v75
	v_add_f32_e32 v75, v177, v75
	v_add_f32_e32 v75, v215, v75
	v_add_f32_e32 v75, v176, v75
	v_mfma_f32_32x32x16_bf16 v[128:143], v[64:67], v[152:155], v[128:143]
	v_add_f32_e32 v75, v178, v75
	v_add_f32_e32 v75, v173, v75
	v_add_f32_e32 v75, v175, v75
	v_add_f32_e32 v75, v171, v75
	v_add_f32_e32 v75, v174, v75
	v_add_f32_e32 v75, v169, v75
	v_add_f32_e32 v75, v172, v75
	s_waitcnt lgkmcnt(3)
	v_mfma_f32_32x32x16_bf16 v[128:143], v[76:79], v[148:151], v[128:143]
	v_add_f32_e32 v75, v168, v75
	v_add_f32_e32 v75, v170, v75
	v_add_f32_e32 v75, v180, v75
	v_add_f32_e32 v75, v182, v75
	v_exp_f32_e32 v64, v102
	v_exp_f32_e32 v65, v103
	v_exp_f32_e32 v66, v104
	s_waitcnt lgkmcnt(2)
	v_mfma_f32_32x32x16_bf16 v[112:127], v[220:223], v[148:151], v[112:127]
	v_exp_f32_e32 v67, v105
	v_exp_f32_e32 v105, v106
	v_exp_f32_e32 v106, v107
	v_exp_f32_e32 v107, v108
	v_exp_f32_e32 v72, v109
	v_exp_f32_e32 v73, v110
	v_exp_f32_e32 v74, v111
	s_waitcnt lgkmcnt(1)
	v_mfma_f32_32x32x16_bf16 v[128:143], v[68:71], v[144:147], v[128:143]
	v_add_f32_e32 v68, v213, v75
	v_add_f32_e32 v68, v214, v68
	v_add_f32_e32 v68, v219, v68
	v_add_f32_e32 v68, v228, v68
	v_add_f32_e32 v68, v64, v68
	v_add_f32_e32 v68, v65, v68
	v_add_f32_e32 v68, v66, v68
	v_add_f32_e32 v68, v67, v68
	s_waitcnt lgkmcnt(0)
	v_mfma_f32_32x32x16_bf16 v[112:127], v[224:227], v[144:147], v[112:127]
	v_add_f32_e32 v68, v105, v68
	v_add_f32_e32 v68, v106, v68
	v_add_f32_e32 v68, v107, v68
	v_add_f32_e32 v68, v72, v68
	v_add_f32_e32 v68, v73, v68
	v_add_f32_e32 v211, v74, v68
	v_mov_b32_e32 v212, v211
	v_cvt_pk_bf16_f32 v108, v173, v175
	v_cvt_pk_bf16_f32 v109, v171, v174
	v_cvt_pk_bf16_f32 v110, v169, v172
	v_cvt_pk_bf16_f32 v111, v168, v170
	v_cvt_pk_bf16_f32 v100, v180, v182
	v_cvt_pk_bf16_f32 v101, v213, v214
	v_cvt_pk_bf16_f32 v102, v219, v228
	v_cvt_pk_bf16_f32 v103, v64, v65
	v_cvt_pk_bf16_f32 v104, v66, v67
	v_cvt_pk_bf16_f32 v105, v105, v106
	v_cvt_pk_bf16_f32 v106, v107, v72
	v_cvt_pk_bf16_f32 v107, v73, v74
	s_nop 1
	v_permlane32_swap_b32_e32 v211, v212
	v_permlane32_swap_b32_e32 v96, v98
	v_permlane32_swap_b32_e32 v97, v99
	v_permlane32_swap_b32_e32 v108, v110
	v_permlane32_swap_b32_e32 v109, v111
	v_permlane32_swap_b32_e32 v100, v102
	v_permlane32_swap_b32_e32 v101, v103
	v_permlane32_swap_b32_e32 v104, v106
	v_permlane32_swap_b32_e32 v105, v107
	s_add_u32 s66, s46, s28
	s_addc_u32 s67, s47, s29
	s_add_u32 s34, s66, 0x23808000
	s_addc_u32 s35, s67, 0
	s_add_u32 s76, s66, 0x2380a000
	s_addc_u32 s77, s67, 0
	s_add_u32 s74, s46, s24
	s_addc_u32 s75, s47, s25
	s_add_u32 s78, s74, 0x21804000
	s_addc_u32 s79, s75, 0
	v_mov_b32_e32 v64, v197
	v_mov_b32_e32 v65, v196
	global_load_dwordx4 v[176:179], v65, s[34:35]
	global_load_dwordx4 v[172:175], v65, s[76:77]
	global_load_dwordx4 v[168:171], v64, s[78:79]
	s_andn2_b64 vcc, exec, s[2:3]
	s_cbranch_vccnz .LBB4_851
	v_mov_b32_e32 v64, v188
	s_mov_b64 s[2:3], s[8:9]
	global_store_dwordx2 v64, v[184:185], s[2:3] nt

; #define AT_SBAR() __builtin_amdgcn_sched_barrier(0)
; template <int OFF> DI s16x4 tr_read(int vb) { s16x4 r; asm volatile("ds_read_b64_tr_b16 %0, %1 offset:%2" : "=&v"(r) : "v"(vb), "i"(OFF) : "memory"); return r; }
; template <int D0> DI void pv_one(f32x16& od, int vb, bf16x8 pa0, bf16x8 pa1, bf16x8 pa2, bf16x8 pa3) {
;     const s16x4 l0 = tr_read<v_rd_off(D0, 0, 0)>(vb), h0 = tr_read<v_rd_off(D0, 0, 1)>(vb), l1 = tr_read<v_rd_off(D0, 1, 0)>(vb), h1 = tr_read<v_rd_off(D0, 1, 1)>(vb);
;     const s16x4 l2 = tr_read<v_rd_off(D0, 2, 0)>(vb), h2 = tr_read<v_rd_off(D0, 2, 1)>(vb), l3 = tr_read<v_rd_off(D0, 3, 0)>(vb), h3 = tr_read<v_rd_off(D0, 3, 1)>(vb);
;     asm volatile("s_waitcnt lgkmcnt(0)" ::: "memory"); AT_SBAR();
;     ...
;     od = __builtin_amdgcn_mfma_f32_32x32x16_bf16(AT_PK(l0, h0), pa0, od, 0, 0, 0);
;     od = __builtin_amdgcn_mfma_f32_32x32x16_bf16(AT_PK(l1, h1), pa1, od, 0, 0, 0);
;     od = __builtin_amdgcn_mfma_f32_32x32x16_bf16(AT_PK(l2, h2), pa2, od, 0, 0, 0);
;     od = __builtin_amdgcn_mfma_f32_32x32x16_bf16(AT_PK(l3, h3), pa3, od, 0, 0, 0);
;     ...
; }
; DI void attn_pass(const Frame& F, CvRide& cv, const bf16_t* __restrict__ Qb, const bf16_t* __restrict__ Kh, const bf16_t* __restrict__ Vh, char* lds, f32x16 (&o)[4], float& l_out, const int wave_s) {
;     ...
;     const unsigned cv_ldo = (unsigned)(((tid >> 4) * 2 * 2048 + (tid & 15) * 4) * 4), cv_sto = (unsigned)((tid >> 3) * 2048 + 8 * (tid & 7));
;     const int cv_lw = OFF_CV + (4 * (tid & 15)) * 68 + 2 * (tid >> 4), cv_lr = OFF_CV + (tid >> 3) * 68 + 8 * (tid & 7);
;     f32x4 cvA = f32x4{}, cvB = f32x4{}; unsigned cvr0 = 0, cvr1 = 0;
.LBB4_853:
	ds_read_b64_tr_b16 v[214:215], v182 offset:0x600
	ds_read_b64_tr_b16 v[216:217], v182 offset:0xe00
	ds_read_b64_tr_b16 v[218:219], v182 offset:0x1600
	ds_read_b64_tr_b16 v[220:221], v182 offset:0x1e00
	ds_read_b64_tr_b16 v[222:223], v182 offset:0x2600
	ds_read_b64_tr_b16 v[224:225], v182 offset:0x2e00
	ds_read_b64_tr_b16 v[226:227], v182 offset:0x3600
	ds_read_b64_tr_b16 v[228:229], v182 offset:0x3e00
	s_waitcnt lgkmcnt(0)
	s_nop 0
	v_mfma_f32_32x32x16_bf16 v[0:15], v[214:217], v[96:99], v[0:15]
	s_lshl_b32 s2, s57, 14
	s_add_i32 s2, s2, 0
	s_lshl_b32 s3, s57, 13
	v_add_u32_e32 v96, s2, v199
	s_sub_i32 s76, s2, s3
	s_waitcnt vmcnt(0)
	v_add_u32_e32 v97, s2, v200
	v_mfma_f32_32x32x16_bf16 v[0:15], v[218:221], v[108:111], v[0:15]
	ds_write_b128 v96, v[176:179]
	v_add_u32_e32 v96, s76, v201
	ds_write_b128 v97, v[172:175]
	ds_write_b128 v96, v[168:171] offset:49152
	s_andn2_b64 s[2:3], exec, s[30:31]
	s_andn2_b64 vcc, exec, s[30:31]
	v_mfma_f32_32x32x16_bf16 v[0:15], v[222:225], v[100:103], v[0:15]
	v_mfma_f32_32x32x16_bf16 v[0:15], v[226:229], v[104:107], v[0:15]
	s_cbranch_vccnz .LBB4_858
	v_mul_f32_e32 v97, 0x44000000, v160
	v_mul_f32_e32 v98, 0x44000000, v164
	v_med3_f32 v97, v97, s56, v210
	v_med3_f32 v98, v98, s56, v210
	v_cvt_pk_fp8_f32 v99, v97, v98
	v_mul_f32_e32 v97, 0x44000000, v161
	v_mul_f32_e32 v98, 0x44000000, v165
	v_med3_f32 v97, v97, s56, v210
	v_med3_f32 v98, v98, s56, v210
	v_cvt_pk_fp8_f32 v100, v97, v98
	v_mul_f32_e32 v97, 0x44000000, v162
	v_mul_f32_e32 v98, 0x44000000, v166
	v_med3_f32 v97, v97, s56, v210
	v_med3_f32 v98, v98, s56, v210
	s_bitcmp1_b32 s58, 0
	v_cvt_pk_fp8_f32 v101, v97, v98
	v_mul_f32_e32 v97, 0x44000000, v163
	v_mul_f32_e32 v98, 0x44000000, v167
	s_cselect_b32 s8, 0x1100, 0
	v_med3_f32 v97, v97, s56, v210
	v_med3_f32 v98, v98, s56, v210
	v_cmp_eq_u32_e32 vcc, 0, v181
	v_add_u32_e32 v96, s8, v190
	v_cvt_pk_fp8_f32 v102, v97, v98
	s_and_b64 vcc, exec, vcc
	s_and_b32 s30, s58, 31
	ds_write_b16 v96, v99
	ds_write_b16 v96, v100 offset:68
	ds_write_b16 v96, v101 offset:136
	ds_write_b16 v96, v102 offset:204
	s_cbranch_vccnz .LBB4_882
	s_lshl_b32 s8, s30, 7
	s_lshl_b32 s9, s58, 6
	s_and_b32 s8, s8, 0xf00
	s_and_b32 s9, s9, 64
	s_or_b32 s26, s8, s9
	s_cbranch_execnz .LBB4_857

; #define AT_SWRITE(b, i) do { *(bf16x8*)(V_lds + (b) * SHM_V + vst0) = sr_[i].vs0; *(bf16x8*)(V_lds + (b) * SHM_V + vst1) = sr_[i].vs1; *(bf16x8*)(K_lds + (b) * SHM_K + kst) = sr_[i].ks0; } while (0)
; DI void attn_pass(const Frame& F, CvRide& cv, const bf16_t* __restrict__ Qb, const bf16_t* __restrict__ Kh, const bf16_t* __restrict__ Vh, char* lds, f32x16 (&o)[4], float& l_out, const int wave_s) {
;     ...
;     f32x16 pA0, pA1, pB0, pB1; float alA, alB; bf16x8 pa0, pa1, pa2, pa3; constexpr int NT = S / 64;
;     constexpr int SE = 0;
;     {
;         bf16x8 v10 = *reinterpret_cast<const bf16x8*>(&Vh[(size_t)(64 + sr) * 128 + sc]), v11 = *reinterpret_cast<const bf16x8*>(&Vh[(size_t)(96 + sr) * 128 + sc]);
;         bf16x8 k10 = *reinterpret_cast<const bf16x8*>(&Kh[(size_t)(64 + kr) * 64 + (tid & 7) * 8]);
;         AT_SLOAD(SE, 0); asm volatile("s_waitcnt vmcnt(0)" ::: "memory");
;         __syncthreads();
;         AT_SWRITE(0, SE);
;         *(bf16x8*)(V_lds + SHM_V + vst0) = v10; *(bf16x8*)(V_lds + SHM_V + vst1) = v11; *(bf16x8*)(K_lds + SHM_K + kst) = k10;
;         __syncthreads();
;     }
;     qkt(pA0, pA1, K_lds, qr, negm, r32, hi); partialSM(pA0, pA1, m_ref, negm, alA);
;     int s_prev = 0, s_cur = 1, s_next = 2;
.LBB4_860:
	s_and_b64 vcc, exec, s[2:3]
	s_waitcnt lgkmcnt(0)
	s_barrier
	v_add_u32_e32 v100, s76, v203
	ds_read_b128 v[96:99], v100 offset:49152
	ds_read_b128 v[168:171], v100 offset:53248
	s_cbranch_vccnz .LBB4_862
	s_andn2_b32 s26, 1, s58
	s_mulk_i32 s26, 0x1100
	v_add_u32_e32 v252, s26, v189
	ds_read2_b32 v[184:185], v252 offset1:1

; DI void finishSM(f32x16& p0, f32x16& p1, float alpha, float& l_reg, bf16x8& pa0, bf16x8& pa1, bf16x8& pa2, bf16x8& pa3) {
; #pragma unroll
;     for (int r = 0; r < 16; ++r) p1[r] = __builtin_amdgcn_exp2f(p1[r]);
;     float ps = 0;
; #pragma unroll
;     for (int r = 0; r < 16; ++r) ps += p0[r];
; #pragma unroll
;     for (int r = 0; r < 16; ++r) ps += p1[r];
;     { auto rr = __builtin_amdgcn_permlane32_swap(__float_as_uint(ps), __float_as_uint(ps), false, false); ps = __uint_as_float(rr[0]) + __uint_as_float(rr[1]); }
;     l_reg = l_reg * alpha + ps;
;     ...
;     AT_PK4(p0, 0, pa0); AT_PK4(p0, 8, pa1); AT_PK4(p1, 0, pa2); AT_PK4(p1, 8, pa3);
;     ...
; }
; DI void qkt(f32x16& p0, f32x16& p1, const char* Ks, const bf16x8* qr, const f32x16& negm, int r32, int hi) {
; #pragma unroll
;     for (int d0 = 0; d0 < 4; ++d0) { const int cb = (d0 * 16 + hi * 8) * 2;
;         const bf16x8 b0 = *reinterpret_cast<const bf16x8*>(Ks + AT_KSWZ(r32, cb));
;         const bf16x8 b1 = *reinterpret_cast<const bf16x8*>(Ks + AT_KSWZ(32 + r32, cb));
;         p0 = __builtin_amdgcn_mfma_f32_32x32x16_bf16(b0, qr[d0], d0 == 0 ? negm : p0, 0, 0, 0);
;         p1 = __builtin_amdgcn_mfma_f32_32x32x16_bf16(b1, qr[d0], d0 == 0 ? negm : p1, 0, 0, 0); }
; }
; DI void attn_pass(const Frame& F, CvRide& cv, const bf16_t* __restrict__ Qb, const bf16_t* __restrict__ Kh, const bf16_t* __restrict__ Vh, char* lds, f32x16 (&o)[4], float& l_out, const int wave_s) {
;     ...
;     const unsigned cv_ldo = (unsigned)(((tid >> 4) * 2 * 2048 + (tid & 15) * 4) * 4), cv_sto = (unsigned)((tid >> 3) * 2048 + 8 * (tid & 7));
;     const int cv_lw = OFF_CV + (4 * (tid & 15)) * 68 + 2 * (tid >> 4), cv_lr = OFF_CV + (tid >> 3) * 68 + 8 * (tid & 7);
;     f32x4 cvA = f32x4{}, cvB = f32x4{}; unsigned cvr0 = 0, cvr1 = 0;
.LBB4_869:
	s_lshl_b32 s26, s58, 8
	s_and_b32 s26, s26, 0x1f00
	s_add_u32 s34, s12, s26
	s_addc_u32 s35, s13, 0
	s_add_u32 s78, s34, 0x2000
	s_addc_u32 s79, s35, 0
	v_mov_b32_e32 v252, v209
	global_load_dwordx4 v[160:163], v252, s[34:35] nt
	global_load_dwordx4 v[164:167], v252, s[78:79] nt
.LBB4_870:
	v_exp_f32_e32 v182, v128
	v_exp_f32_e32 v230, v129
	v_exp_f32_e32 v231, v130
	v_exp_f32_e32 v232, v131
	v_exp_f32_e32 v233, v132
	v_exp_f32_e32 v234, v133
	v_exp_f32_e32 v235, v134
	v_exp_f32_e32 v236, v135
	v_exp_f32_e32 v237, v136
	v_exp_f32_e32 v238, v137
	v_exp_f32_e32 v239, v138
	v_exp_f32_e32 v240, v139
	v_exp_f32_e32 v241, v140
	v_exp_f32_e32 v242, v141
	v_exp_f32_e32 v243, v142
	v_exp_f32_e32 v244, v143
	v_add_u32_e32 v101, s76, v204
	v_add_u32_e32 v102, s76, v205
	v_add_u32_e32 v103, s76, v206
	ds_read_b128 v[172:175], v101 offset:49152
	ds_read_b128 v[176:179], v101 offset:53248
	ds_read_b128 v[214:217], v102 offset:49152
	ds_read_b128 v[218:221], v102 offset:53248
	ds_read_b128 v[222:225], v103 offset:49152
	ds_read_b128 v[226:229], v103 offset:53248
	v_exp_f32_e32 v112, v112
	v_exp_f32_e32 v113, v113
	v_exp_f32_e32 v114, v114
	s_waitcnt lgkmcnt(7)
	v_mfma_f32_32x32x16_bf16 v[128:143], v[96:99], v[156:159], v[80:95]
	v_exp_f32_e32 v115, v115
	v_exp_f32_e32 v116, v116
	v_exp_f32_e32 v117, v117
	v_exp_f32_e32 v118, v118
	v_exp_f32_e32 v119, v119
	s_waitcnt lgkmcnt(6)
	v_mfma_f32_32x32x16_bf16 v[96:111], v[168:171], v[156:159], v[80:95]
	v_exp_f32_e32 v168, v120
	v_add_f32_e32 v120, 0, v182
	v_add_f32_e32 v120, v230, v120
	v_add_f32_e32 v120, v231, v120
	v_add_f32_e32 v120, v232, v120
	v_add_f32_e32 v120, v233, v120
	v_add_f32_e32 v120, v234, v120
	v_add_f32_e32 v120, v235, v120
	v_add_f32_e32 v120, v236, v120
	v_add_f32_e32 v120, v237, v120
	v_add_f32_e32 v120, v238, v120
	s_waitcnt lgkmcnt(5)
	v_mfma_f32_32x32x16_bf16 v[128:143], v[172:175], v[152:155], v[128:143]
	v_add_f32_e32 v120, v239, v120
	v_add_f32_e32 v120, v240, v120
	v_add_f32_e32 v120, v241, v120
	v_add_f32_e32 v120, v242, v120
	v_add_f32_e32 v120, v243, v120
	v_add_f32_e32 v120, v244, v120
	v_add_f32_e32 v120, v112, v120
	s_waitcnt lgkmcnt(4)
	v_mfma_f32_32x32x16_bf16 v[96:111], v[176:179], v[152:155], v[96:111]
	v_add_f32_e32 v120, v113, v120
	v_add_f32_e32 v120, v114, v120
	v_add_f32_e32 v120, v115, v120
	v_add_f32_e32 v120, v116, v120
	v_exp_f32_e32 v169, v121
	v_add_f32_e32 v120, v117, v120
	v_exp_f32_e32 v170, v122
	s_waitcnt lgkmcnt(3)
	v_mfma_f32_32x32x16_bf16 v[128:143], v[214:217], v[148:151], v[128:143]
	v_add_f32_e32 v120, v118, v120
	v_exp_f32_e32 v171, v123
	v_add_f32_e32 v120, v119, v120
	v_exp_f32_e32 v172, v124
	v_add_f32_e32 v120, v168, v120
	v_exp_f32_e32 v173, v125
	v_add_f32_e32 v120, v169, v120
	s_waitcnt lgkmcnt(2)
	v_mfma_f32_32x32x16_bf16 v[96:111], v[218:221], v[148:151], v[96:111]
	v_exp_f32_e32 v174, v126
	v_add_f32_e32 v120, v170, v120
	v_exp_f32_e32 v175, v127
	v_add_f32_e32 v120, v171, v120
	v_add_f32_e32 v120, v172, v120
	v_add_f32_e32 v120, v173, v120
	v_add_f32_e32 v120, v174, v120
	s_waitcnt lgkmcnt(1)
	v_mfma_f32_32x32x16_bf16 v[128:143], v[222:225], v[144:147], v[128:143]
	v_add_f32_e32 v213, v175, v120
	v_mov_b32_e32 v214, v213
	v_cvt_pk_bf16_f32 v120, v182, v230
	v_cvt_pk_bf16_f32 v121, v231, v232
	v_cvt_pk_bf16_f32 v122, v233, v234
	v_cvt_pk_bf16_f32 v123, v235, v236
	v_cvt_pk_bf16_f32 v124, v237, v238
	s_waitcnt lgkmcnt(0)
	v_mfma_f32_32x32x16_bf16 v[96:111], v[226:229], v[144:147], v[96:111]
	v_cvt_pk_bf16_f32 v125, v239, v240
	v_cvt_pk_bf16_f32 v126, v241, v242
	v_cvt_pk_bf16_f32 v127, v243, v244
	v_cvt_pk_bf16_f32 v112, v112, v113
	v_cvt_pk_bf16_f32 v113, v114, v115
	v_cvt_pk_bf16_f32 v114, v116, v117
	v_cvt_pk_bf16_f32 v115, v118, v119
	v_cvt_pk_bf16_f32 v116, v168, v169
	v_cvt_pk_bf16_f32 v117, v170, v171
	v_cvt_pk_bf16_f32 v118, v172, v173
	v_cvt_pk_bf16_f32 v119, v174, v175
	v_permlane32_swap_b32_e32 v213, v214
	v_permlane32_swap_b32_e32 v120, v122
	v_permlane32_swap_b32_e32 v121, v123
	v_permlane32_swap_b32_e32 v124, v126
	v_permlane32_swap_b32_e32 v125, v127
	v_permlane32_swap_b32_e32 v112, v114
	v_permlane32_swap_b32_e32 v113, v115
	v_permlane32_swap_b32_e32 v116, v118
	v_permlane32_swap_b32_e32 v117, v119
	s_add_u32 s34, s66, 0x2380c000
	s_addc_u32 s35, s67, 0
	s_add_u32 s66, s66, 0x2380e000
	s_addc_u32 s67, s67, 0
	s_add_u32 s74, s74, 0x21806000
	s_addc_u32 s75, s75, 0
	v_mov_b32_e32 v168, v197
	v_mov_b32_e32 v169, v196
	global_load_dwordx4 v[176:179], v169, s[34:35]
	global_load_dwordx4 v[172:175], v169, s[66:67]
	s_nop 0
	global_load_dwordx4 v[168:171], v168, s[74:75]
	s_and_b64 vcc, exec, s[2:3]
	s_cbranch_vccnz .LBB4_872
	v_mov_b32_e32 v182, v188
	s_mov_b64 s[2:3], s[8:9]
	global_store_dwordx2 v182, v[184:185], s[2:3] nt

; #define AT_SWRITE(b, i) do { *(bf16x8*)(V_lds + (b) * SHM_V + vst0) = sr_[i].vs0; *(bf16x8*)(V_lds + (b) * SHM_V + vst1) = sr_[i].vs1; *(bf16x8*)(K_lds + (b) * SHM_K + kst) = sr_[i].ks0; } while (0)
; DI void qkt(f32x16& p0, f32x16& p1, const char* Ks, const bf16x8* qr, const f32x16& negm, int r32, int hi) {
; #pragma unroll
;     for (int d0 = 0; d0 < 4; ++d0) { const int cb = (d0 * 16 + hi * 8) * 2;
;         const bf16x8 b0 = *reinterpret_cast<const bf16x8*>(Ks + AT_KSWZ(r32, cb));
;         const bf16x8 b1 = *reinterpret_cast<const bf16x8*>(Ks + AT_KSWZ(32 + r32, cb));
;         p0 = __builtin_amdgcn_mfma_f32_32x32x16_bf16(b0, qr[d0], d0 == 0 ? negm : p0, 0, 0, 0);
;         p1 = __builtin_amdgcn_mfma_f32_32x32x16_bf16(b1, qr[d0], d0 == 0 ? negm : p1, 0, 0, 0); }
; }
; DI void attn_pass(const Frame& F, CvRide& cv, const bf16_t* __restrict__ Qb, const bf16_t* __restrict__ Kh, const bf16_t* __restrict__ Vh, char* lds, f32x16 (&o)[4], float& l_out, const int wave_s) {
;     ...
;     f32x16 pA0, pA1, pB0, pB1; float alA, alB; bf16x8 pa0, pa1, pa2, pa3; constexpr int NT = S / 64;
;     constexpr int SE = 0;
;     {
;         bf16x8 v10 = *reinterpret_cast<const bf16x8*>(&Vh[(size_t)(64 + sr) * 128 + sc]), v11 = *reinterpret_cast<const bf16x8*>(&Vh[(size_t)(96 + sr) * 128 + sc]);
;         bf16x8 k10 = *reinterpret_cast<const bf16x8*>(&Kh[(size_t)(64 + kr) * 64 + (tid & 7) * 8]);
;         AT_SLOAD(SE, 0); asm volatile("s_waitcnt vmcnt(0)" ::: "memory");
;         __syncthreads();
;         AT_SWRITE(0, SE);
;         *(bf16x8*)(V_lds + SHM_V + vst0) = v10; *(bf16x8*)(V_lds + SHM_V + vst1) = v11; *(bf16x8*)(K_lds + SHM_K + kst) = k10;
;         __syncthreads();
;     }
;     qkt(pA0, pA1, K_lds, qr, negm, r32, hi); partialSM(pA0, pA1, m_ref, negm, alA);
;     int s_prev = 0, s_cur = 1, s_next = 2;
.LBB4_913:
	s_lshl_b32 s92, s29, 13
	v_add_u32_e32 v68, s92, v207
	ds_read_b128 v[64:67], v68 offset:49152
	ds_read_b128 v[68:71], v68 offset:53248
	s_cmp_lg_u32 s18, 0
	s_mov_b32 s30, s29
	s_cselect_b64 s[2:3], -1, 0
	s_cmp_eq_u32 s18, 0
	s_mov_b32 s29, s22
	s_cbranch_scc1 .LBB4_915
	s_andn2_b32 s18, 1, s58
	s_mulk_i32 s18, 0x1100
	v_add_u32_e32 v252, s18, v194
	ds_read2_b32 v[184:185], v252 offset1:1

; DI void finishSM(f32x16& p0, f32x16& p1, float alpha, float& l_reg, bf16x8& pa0, bf16x8& pa1, bf16x8& pa2, bf16x8& pa3) {
; #pragma unroll
;     for (int r = 0; r < 16; ++r) p1[r] = __builtin_amdgcn_exp2f(p1[r]);
;     float ps = 0;
; #pragma unroll
;     for (int r = 0; r < 16; ++r) ps += p0[r];
; #pragma unroll
;     for (int r = 0; r < 16; ++r) ps += p1[r];
;     { auto rr = __builtin_amdgcn_permlane32_swap(__float_as_uint(ps), __float_as_uint(ps), false, false); ps = __uint_as_float(rr[0]) + __uint_as_float(rr[1]); }
;     l_reg = l_reg * alpha + ps;
;     ...
;     AT_PK4(p0, 0, pa0); AT_PK4(p0, 8, pa1); AT_PK4(p1, 0, pa2); AT_PK4(p1, 8, pa3);
;     ...
; }
; DI void qkt(f32x16& p0, f32x16& p1, const char* Ks, const bf16x8* qr, const f32x16& negm, int r32, int hi) {
; #pragma unroll
;     for (int d0 = 0; d0 < 4; ++d0) { const int cb = (d0 * 16 + hi * 8) * 2;
;         const bf16x8 b0 = *reinterpret_cast<const bf16x8*>(Ks + AT_KSWZ(r32, cb));
;         const bf16x8 b1 = *reinterpret_cast<const bf16x8*>(Ks + AT_KSWZ(32 + r32, cb));
;         p0 = __builtin_amdgcn_mfma_f32_32x32x16_bf16(b0, qr[d0], d0 == 0 ? negm : p0, 0, 0, 0);
;         p1 = __builtin_amdgcn_mfma_f32_32x32x16_bf16(b1, qr[d0], d0 == 0 ? negm : p1, 0, 0, 0); }
; }
; DI void attn_pass(const Frame& F, CvRide& cv, const bf16_t* __restrict__ Qb, const bf16_t* __restrict__ Kh, const bf16_t* __restrict__ Vh, char* lds, f32x16 (&o)[4], float& l_out, const int wave_s) {
;     ...
;     const unsigned cv_ldo = (unsigned)(((tid >> 4) * 2 * 2048 + (tid & 15) * 4) * 4), cv_sto = (unsigned)((tid >> 3) * 2048 + 8 * (tid & 7));
;     const int cv_lw = OFF_CV + (4 * (tid & 15)) * 68 + 2 * (tid >> 4), cv_lr = OFF_CV + (tid >> 3) * 68 + 8 * (tid & 7);
;     f32x4 cvA = f32x4{}, cvB = f32x4{}; unsigned cvr0 = 0, cvr1 = 0;
.LBB4_922:
	s_lshl_b32 s18, s58, 8
	s_and_b32 s18, s18, 0x1f00
	s_add_u32 s24, s12, s18
	s_addc_u32 s25, s13, 0
	s_add_u32 s34, s24, 0x2000
	s_addc_u32 s35, s25, 0
	v_mov_b32_e32 v252, v213
	global_load_dwordx4 v[160:163], v252, s[24:25] nt
	global_load_dwordx4 v[164:167], v252, s[34:35] nt
.LBB4_923:
	s_lshl_b32 s18, s30, 13
	s_add_i32 s18, s18, 0
	v_add_u32_e32 v72, s18, v208
	v_add_u32_e32 v112, s18, v209
	v_add_u32_e32 v180, s18, v210
	s_waitcnt lgkmcnt(1)
	v_mfma_f32_32x32x16_bf16 v[128:143], v[64:67], v[156:159], v[80:95]
	ds_read_b128 v[64:67], v72 offset:49152
	ds_read_b128 v[72:75], v72 offset:53248
	ds_read_b128 v[76:79], v112 offset:49152
	ds_read_b128 v[224:227], v112 offset:53248
	v_exp_f32_e32 v182, v97
	v_exp_f32_e32 v217, v98
	v_exp_f32_e32 v218, v99
	v_exp_f32_e32 v223, v100
	v_exp_f32_e32 v232, v101
	s_waitcnt lgkmcnt(4)
	v_mfma_f32_32x32x16_bf16 v[112:127], v[68:71], v[156:159], v[80:95]
	ds_read_b128 v[68:71], v180 offset:49152
	ds_read_b128 v[228:231], v180 offset:53248
	v_exp_f32_e32 v180, v96
	v_cvt_pk_bf16_f32 v96, v220, v222
	v_cvt_pk_bf16_f32 v97, v179, v221
	v_cvt_pk_bf16_f32 v98, v177, v219
	v_cvt_pk_bf16_f32 v99, v176, v178
	s_waitcnt lgkmcnt(4)
	v_mfma_f32_32x32x16_bf16 v[112:127], v[72:75], v[152:155], v[112:127]
	v_add_f32_e32 v75, 0, v220
	v_add_f32_e32 v75, v222, v75
	v_add_f32_e32 v75, v179, v75
	v_add_f32_e32 v75, v221, v75
	v_add_f32_e32 v75, v177, v75
	v_add_f32_e32 v75, v219, v75
	v_add_f32_e32 v75, v176, v75
	v_mfma_f32_32x32x16_bf16 v[128:143], v[64:67], v[152:155], v[128:143]
	v_add_f32_e32 v75, v178, v75
	v_add_f32_e32 v75, v173, v75
	v_add_f32_e32 v75, v175, v75
	v_add_f32_e32 v75, v171, v75
	v_add_f32_e32 v75, v174, v75
	v_add_f32_e32 v75, v169, v75
	v_add_f32_e32 v75, v172, v75
	s_waitcnt lgkmcnt(3)
	v_mfma_f32_32x32x16_bf16 v[128:143], v[76:79], v[148:151], v[128:143]
	v_add_f32_e32 v75, v168, v75
	v_add_f32_e32 v75, v170, v75
	v_add_f32_e32 v75, v180, v75
	v_add_f32_e32 v75, v182, v75
	v_exp_f32_e32 v64, v102
	v_exp_f32_e32 v65, v103
	v_exp_f32_e32 v66, v104
	s_waitcnt lgkmcnt(2)
	v_mfma_f32_32x32x16_bf16 v[112:127], v[224:227], v[148:151], v[112:127]
	v_exp_f32_e32 v67, v105
	v_exp_f32_e32 v105, v106
	v_exp_f32_e32 v106, v107
	v_exp_f32_e32 v107, v108
	v_exp_f32_e32 v72, v109
	v_exp_f32_e32 v73, v110
	v_exp_f32_e32 v74, v111
	s_waitcnt lgkmcnt(1)
	v_mfma_f32_32x32x16_bf16 v[128:143], v[68:71], v[144:147], v[128:143]
	v_add_f32_e32 v68, v217, v75
	v_add_f32_e32 v68, v218, v68
	v_add_f32_e32 v68, v223, v68
	v_add_f32_e32 v68, v232, v68
	v_add_f32_e32 v68, v64, v68
	v_add_f32_e32 v68, v65, v68
	v_add_f32_e32 v68, v66, v68
	v_add_f32_e32 v68, v67, v68
	s_waitcnt lgkmcnt(0)
	v_mfma_f32_32x32x16_bf16 v[112:127], v[228:231], v[144:147], v[112:127]
	v_add_f32_e32 v68, v105, v68
	v_add_f32_e32 v68, v106, v68
	v_add_f32_e32 v68, v107, v68
	v_add_f32_e32 v68, v72, v68
	v_add_f32_e32 v68, v73, v68
	v_add_f32_e32 v215, v74, v68
	v_mov_b32_e32 v216, v215
	v_cvt_pk_bf16_f32 v108, v173, v175
	v_cvt_pk_bf16_f32 v109, v171, v174
	v_cvt_pk_bf16_f32 v110, v169, v172
	v_cvt_pk_bf16_f32 v111, v168, v170
	v_cvt_pk_bf16_f32 v100, v180, v182
	v_cvt_pk_bf16_f32 v101, v217, v218
	v_cvt_pk_bf16_f32 v102, v223, v232
	v_cvt_pk_bf16_f32 v103, v64, v65
	v_cvt_pk_bf16_f32 v104, v66, v67
	v_cvt_pk_bf16_f32 v105, v105, v106
	v_cvt_pk_bf16_f32 v106, v107, v72
	v_cvt_pk_bf16_f32 v107, v73, v74
	s_nop 1
	v_permlane32_swap_b32_e32 v215, v216
	v_permlane32_swap_b32_e32 v96, v98
	v_permlane32_swap_b32_e32 v97, v99
	v_permlane32_swap_b32_e32 v108, v110
	v_permlane32_swap_b32_e32 v109, v111
	v_permlane32_swap_b32_e32 v100, v102
	v_permlane32_swap_b32_e32 v101, v103
	v_permlane32_swap_b32_e32 v104, v106
	v_permlane32_swap_b32_e32 v105, v107
	s_add_u32 s34, s46, s16
	s_addc_u32 s35, s47, s17
	s_add_u32 s24, s34, 0x23808000
	s_addc_u32 s25, s35, 0
	s_add_u32 s54, s34, 0x2380a000
	s_addc_u32 s55, s35, 0
	s_add_u32 s42, s46, s20
	s_addc_u32 s43, s47, s21
	s_add_u32 s56, s42, 0x21884000
	s_addc_u32 s57, s43, 0
	v_mov_b32_e32 v64, v201
	v_mov_b32_e32 v65, v200
	global_load_dwordx4 v[176:179], v65, s[24:25]
	global_load_dwordx4 v[172:175], v65, s[54:55]
	global_load_dwordx4 v[168:171], v64, s[56:57]
	s_andn2_b64 vcc, exec, s[2:3]
	s_cbranch_vccnz .LBB4_925
	v_mov_b32_e32 v64, v193
	s_mov_b64 s[2:3], s[8:9]
	global_store_dwordx2 v64, v[184:185], s[2:3] nt

; #define AT_SBAR() __builtin_amdgcn_sched_barrier(0)
; template <int OFF> DI s16x4 tr_read(int vb) { s16x4 r; asm volatile("ds_read_b64_tr_b16 %0, %1 offset:%2" : "=&v"(r) : "v"(vb), "i"(OFF) : "memory"); return r; }
; template <int D0> DI void pv_one(f32x16& od, int vb, bf16x8 pa0, bf16x8 pa1, bf16x8 pa2, bf16x8 pa3) {
;     const s16x4 l0 = tr_read<v_rd_off(D0, 0, 0)>(vb), h0 = tr_read<v_rd_off(D0, 0, 1)>(vb), l1 = tr_read<v_rd_off(D0, 1, 0)>(vb), h1 = tr_read<v_rd_off(D0, 1, 1)>(vb);
;     const s16x4 l2 = tr_read<v_rd_off(D0, 2, 0)>(vb), h2 = tr_read<v_rd_off(D0, 2, 1)>(vb), l3 = tr_read<v_rd_off(D0, 3, 0)>(vb), h3 = tr_read<v_rd_off(D0, 3, 1)>(vb);
;     asm volatile("s_waitcnt lgkmcnt(0)" ::: "memory"); AT_SBAR();
;     ...
;     od = __builtin_amdgcn_mfma_f32_32x32x16_bf16(AT_PK(l0, h0), pa0, od, 0, 0, 0);
;     od = __builtin_amdgcn_mfma_f32_32x32x16_bf16(AT_PK(l1, h1), pa1, od, 0, 0, 0);
;     od = __builtin_amdgcn_mfma_f32_32x32x16_bf16(AT_PK(l2, h2), pa2, od, 0, 0, 0);
;     od = __builtin_amdgcn_mfma_f32_32x32x16_bf16(AT_PK(l3, h3), pa3, od, 0, 0, 0);
;     ...
; }
; DI void attn_pass(const Frame& F, CvRide& cv, const bf16_t* __restrict__ Qb, const bf16_t* __restrict__ Kh, const bf16_t* __restrict__ Vh, char* lds, f32x16 (&o)[4], float& l_out, const int wave_s) {
;     ...
;     const unsigned cv_ldo = (unsigned)(((tid >> 4) * 2 * 2048 + (tid & 15) * 4) * 4), cv_sto = (unsigned)((tid >> 3) * 2048 + 8 * (tid & 7));
;     const int cv_lw = OFF_CV + (4 * (tid & 15)) * 68 + 2 * (tid >> 4), cv_lr = OFF_CV + (tid >> 3) * 68 + 8 * (tid & 7);
;     f32x4 cvA = f32x4{}, cvB = f32x4{}; unsigned cvr0 = 0, cvr1 = 0;
.LBB4_927:
	ds_read_b64_tr_b16 v[218:219], v182 offset:0x600
	ds_read_b64_tr_b16 v[220:221], v182 offset:0xe00
	ds_read_b64_tr_b16 v[222:223], v182 offset:0x1600
	ds_read_b64_tr_b16 v[224:225], v182 offset:0x1e00
	ds_read_b64_tr_b16 v[226:227], v182 offset:0x2600
	ds_read_b64_tr_b16 v[228:229], v182 offset:0x2e00
	ds_read_b64_tr_b16 v[230:231], v182 offset:0x3600
	ds_read_b64_tr_b16 v[232:233], v182 offset:0x3e00
	s_waitcnt lgkmcnt(0)
	s_nop 0
	v_mfma_f32_32x32x16_bf16 v[0:15], v[218:221], v[96:99], v[0:15]
	s_lshl_b32 s2, s15, 14
	s_add_i32 s2, s2, 0
	s_lshl_b32 s3, s15, 13
	v_add_u32_e32 v96, s2, v203
	s_sub_i32 s54, s2, s3
	s_waitcnt vmcnt(0)
	v_add_u32_e32 v97, s2, v204
	v_mfma_f32_32x32x16_bf16 v[0:15], v[222:225], v[108:111], v[0:15]
	ds_write_b128 v96, v[176:179]
	v_add_u32_e32 v96, s54, v205
	ds_write_b128 v97, v[172:175]
	ds_write_b128 v96, v[168:171] offset:49152
	s_andn2_b64 s[2:3], exec, s[22:23]
	s_andn2_b64 vcc, exec, s[22:23]
	v_mfma_f32_32x32x16_bf16 v[0:15], v[226:229], v[100:103], v[0:15]
	v_mfma_f32_32x32x16_bf16 v[0:15], v[230:233], v[104:107], v[0:15]
	s_cbranch_vccnz .LBB4_932
	v_mul_f32_e32 v97, 0x44000000, v160
	v_mul_f32_e32 v98, 0x44000000, v164
	v_med3_f32 v97, v97, s28, v214
	v_med3_f32 v98, v98, s28, v214
	v_cvt_pk_fp8_f32 v99, v97, v98
	v_mul_f32_e32 v97, 0x44000000, v161
	v_mul_f32_e32 v98, 0x44000000, v165
	v_med3_f32 v97, v97, s28, v214
	v_med3_f32 v98, v98, s28, v214
	v_cvt_pk_fp8_f32 v100, v97, v98
	v_mul_f32_e32 v97, 0x44000000, v162
	v_mul_f32_e32 v98, 0x44000000, v166
	v_med3_f32 v97, v97, s28, v214
	v_med3_f32 v98, v98, s28, v214
	s_bitcmp1_b32 s58, 0
	v_cvt_pk_fp8_f32 v101, v97, v98
	v_mul_f32_e32 v97, 0x44000000, v163
	v_mul_f32_e32 v98, 0x44000000, v167
	s_cselect_b32 s8, 0x1100, 0
	v_med3_f32 v97, v97, s28, v214
	v_med3_f32 v98, v98, s28, v214
	v_cmp_eq_u32_e32 vcc, 0, v181
	v_add_u32_e32 v96, s8, v195
	v_cvt_pk_fp8_f32 v102, v97, v98
	s_and_b64 vcc, exec, vcc
	s_and_b32 s22, s58, 31
	ds_write_b16 v96, v99
	ds_write_b16 v96, v100 offset:68
	ds_write_b16 v96, v101 offset:136
	ds_write_b16 v96, v102 offset:204
	s_cbranch_vccnz .LBB4_956
	s_lshl_b32 s8, s22, 7
	s_lshl_b32 s9, s58, 6
	s_and_b32 s8, s8, 0xf00
	s_and_b32 s9, s9, 64
	s_or_b32 s18, s8, s9
	s_cbranch_execnz .LBB4_931

; #define AT_SWRITE(b, i) do { *(bf16x8*)(V_lds + (b) * SHM_V + vst0) = sr_[i].vs0; *(bf16x8*)(V_lds + (b) * SHM_V + vst1) = sr_[i].vs1; *(bf16x8*)(K_lds + (b) * SHM_K + kst) = sr_[i].ks0; } while (0)
; DI void attn_pass(const Frame& F, CvRide& cv, const bf16_t* __restrict__ Qb, const bf16_t* __restrict__ Kh, const bf16_t* __restrict__ Vh, char* lds, f32x16 (&o)[4], float& l_out, const int wave_s) {
;     ...
;     f32x16 pA0, pA1, pB0, pB1; float alA, alB; bf16x8 pa0, pa1, pa2, pa3; constexpr int NT = S / 64;
;     constexpr int SE = 0;
;     {
;         bf16x8 v10 = *reinterpret_cast<const bf16x8*>(&Vh[(size_t)(64 + sr) * 128 + sc]), v11 = *reinterpret_cast<const bf16x8*>(&Vh[(size_t)(96 + sr) * 128 + sc]);
;         bf16x8 k10 = *reinterpret_cast<const bf16x8*>(&Kh[(size_t)(64 + kr) * 64 + (tid & 7) * 8]);
;         AT_SLOAD(SE, 0); asm volatile("s_waitcnt vmcnt(0)" ::: "memory");
;         __syncthreads();
;         AT_SWRITE(0, SE);
;         *(bf16x8*)(V_lds + SHM_V + vst0) = v10; *(bf16x8*)(V_lds + SHM_V + vst1) = v11; *(bf16x8*)(K_lds + SHM_K + kst) = k10;
;         __syncthreads();
;     }
;     qkt(pA0, pA1, K_lds, qr, negm, r32, hi); partialSM(pA0, pA1, m_ref, negm, alA);
;     int s_prev = 0, s_cur = 1, s_next = 2;
.LBB4_934:
	s_and_b64 vcc, exec, s[2:3]
	s_waitcnt lgkmcnt(0)
	s_barrier
	v_add_u32_e32 v100, s54, v207
	ds_read_b128 v[96:99], v100 offset:49152
	ds_read_b128 v[168:171], v100 offset:53248
	s_cbranch_vccnz .LBB4_936
	s_andn2_b32 s18, 1, s58
	s_mulk_i32 s18, 0x1100
	v_add_u32_e32 v252, s18, v194
	ds_read2_b32 v[184:185], v252 offset1:1

; DI void finishSM(f32x16& p0, f32x16& p1, float alpha, float& l_reg, bf16x8& pa0, bf16x8& pa1, bf16x8& pa2, bf16x8& pa3) {
; #pragma unroll
;     for (int r = 0; r < 16; ++r) p1[r] = __builtin_amdgcn_exp2f(p1[r]);
;     float ps = 0;
; #pragma unroll
;     for (int r = 0; r < 16; ++r) ps += p0[r];
; #pragma unroll
;     for (int r = 0; r < 16; ++r) ps += p1[r];
;     { auto rr = __builtin_amdgcn_permlane32_swap(__float_as_uint(ps), __float_as_uint(ps), false, false); ps = __uint_as_float(rr[0]) + __uint_as_float(rr[1]); }
;     l_reg = l_reg * alpha + ps;
;     ...
;     AT_PK4(p0, 0, pa0); AT_PK4(p0, 8, pa1); AT_PK4(p1, 0, pa2); AT_PK4(p1, 8, pa3);
;     ...
; }
; DI void qkt(f32x16& p0, f32x16& p1, const char* Ks, const bf16x8* qr, const f32x16& negm, int r32, int hi) {
; #pragma unroll
;     for (int d0 = 0; d0 < 4; ++d0) { const int cb = (d0 * 16 + hi * 8) * 2;
;         const bf16x8 b0 = *reinterpret_cast<const bf16x8*>(Ks + AT_KSWZ(r32, cb));
;         const bf16x8 b1 = *reinterpret_cast<const bf16x8*>(Ks + AT_KSWZ(32 + r32, cb));
;         p0 = __builtin_amdgcn_mfma_f32_32x32x16_bf16(b0, qr[d0], d0 == 0 ? negm : p0, 0, 0, 0);
;         p1 = __builtin_amdgcn_mfma_f32_32x32x16_bf16(b1, qr[d0], d0 == 0 ? negm : p1, 0, 0, 0); }
; }
; DI void attn_pass(const Frame& F, CvRide& cv, const bf16_t* __restrict__ Qb, const bf16_t* __restrict__ Kh, const bf16_t* __restrict__ Vh, char* lds, f32x16 (&o)[4], float& l_out, const int wave_s) {
;     ...
;     const unsigned cv_ldo = (unsigned)(((tid >> 4) * 2 * 2048 + (tid & 15) * 4) * 4), cv_sto = (unsigned)((tid >> 3) * 2048 + 8 * (tid & 7));
;     const int cv_lw = OFF_CV + (4 * (tid & 15)) * 68 + 2 * (tid >> 4), cv_lr = OFF_CV + (tid >> 3) * 68 + 8 * (tid & 7);
;     f32x4 cvA = f32x4{}, cvB = f32x4{}; unsigned cvr0 = 0, cvr1 = 0;
.LBB4_943:
	s_lshl_b32 s18, s58, 8
	s_and_b32 s18, s18, 0x1f00
	s_add_u32 s24, s12, s18
	s_addc_u32 s25, s13, 0
	s_add_u32 s56, s24, 0x2000
	s_addc_u32 s57, s25, 0
	v_mov_b32_e32 v252, v213
	global_load_dwordx4 v[160:163], v252, s[24:25] nt
	global_load_dwordx4 v[164:167], v252, s[56:57] nt
.LBB4_944:
	v_exp_f32_e32 v182, v128
	v_exp_f32_e32 v234, v129
	v_exp_f32_e32 v235, v130
	v_exp_f32_e32 v236, v131
	v_exp_f32_e32 v237, v132
	v_exp_f32_e32 v238, v133
	v_exp_f32_e32 v239, v134
	v_exp_f32_e32 v240, v135
	v_exp_f32_e32 v241, v136
	v_exp_f32_e32 v242, v137
	v_exp_f32_e32 v243, v138
	v_exp_f32_e32 v244, v139
	v_exp_f32_e32 v245, v140
	v_exp_f32_e32 v246, v141
	v_exp_f32_e32 v247, v142
	v_exp_f32_e32 v248, v143
	v_add_u32_e32 v101, s54, v208
	v_add_u32_e32 v102, s54, v209
	v_add_u32_e32 v103, s54, v210
	ds_read_b128 v[172:175], v101 offset:49152
	ds_read_b128 v[176:179], v101 offset:53248
	ds_read_b128 v[218:221], v102 offset:49152
	ds_read_b128 v[222:225], v102 offset:53248
	ds_read_b128 v[226:229], v103 offset:49152
	ds_read_b128 v[230:233], v103 offset:53248
	v_exp_f32_e32 v112, v112
	v_exp_f32_e32 v113, v113
	v_exp_f32_e32 v114, v114
	s_waitcnt lgkmcnt(7)
	v_mfma_f32_32x32x16_bf16 v[128:143], v[96:99], v[156:159], v[80:95]
	v_exp_f32_e32 v115, v115
	v_exp_f32_e32 v116, v116
	v_exp_f32_e32 v117, v117
	v_exp_f32_e32 v118, v118
	v_exp_f32_e32 v119, v119
	s_waitcnt lgkmcnt(6)
	v_mfma_f32_32x32x16_bf16 v[96:111], v[168:171], v[156:159], v[80:95]
	v_exp_f32_e32 v168, v120
	v_add_f32_e32 v120, 0, v182
	v_add_f32_e32 v120, v234, v120
	v_add_f32_e32 v120, v235, v120
	v_add_f32_e32 v120, v236, v120
	v_add_f32_e32 v120, v237, v120
	v_add_f32_e32 v120, v238, v120
	v_add_f32_e32 v120, v239, v120
	v_add_f32_e32 v120, v240, v120
	v_add_f32_e32 v120, v241, v120
	v_add_f32_e32 v120, v242, v120
	s_waitcnt lgkmcnt(5)
	v_mfma_f32_32x32x16_bf16 v[128:143], v[172:175], v[152:155], v[128:143]
	v_add_f32_e32 v120, v243, v120
	v_add_f32_e32 v120, v244, v120
	v_add_f32_e32 v120, v245, v120
	v_add_f32_e32 v120, v246, v120
	v_add_f32_e32 v120, v247, v120
	v_add_f32_e32 v120, v248, v120
	v_add_f32_e32 v120, v112, v120
	s_waitcnt lgkmcnt(4)
	v_mfma_f32_32x32x16_bf16 v[96:111], v[176:179], v[152:155], v[96:111]
	v_add_f32_e32 v120, v113, v120
	v_add_f32_e32 v120, v114, v120
	v_add_f32_e32 v120, v115, v120
	v_add_f32_e32 v120, v116, v120
	v_exp_f32_e32 v169, v121
	v_add_f32_e32 v120, v117, v120
	v_exp_f32_e32 v170, v122
	s_waitcnt lgkmcnt(3)
	v_mfma_f32_32x32x16_bf16 v[128:143], v[218:221], v[148:151], v[128:143]
	v_add_f32_e32 v120, v118, v120
	v_exp_f32_e32 v171, v123
	v_add_f32_e32 v120, v119, v120
	v_exp_f32_e32 v172, v124
	v_add_f32_e32 v120, v168, v120
	v_exp_f32_e32 v173, v125
	v_add_f32_e32 v120, v169, v120
	s_waitcnt lgkmcnt(2)
	v_mfma_f32_32x32x16_bf16 v[96:111], v[222:225], v[148:151], v[96:111]
	v_exp_f32_e32 v174, v126
	v_add_f32_e32 v120, v170, v120
	v_exp_f32_e32 v175, v127
	v_add_f32_e32 v120, v171, v120
	v_add_f32_e32 v120, v172, v120
	v_add_f32_e32 v120, v173, v120
	v_add_f32_e32 v120, v174, v120
	s_waitcnt lgkmcnt(1)
	v_mfma_f32_32x32x16_bf16 v[128:143], v[226:229], v[144:147], v[128:143]
	v_add_f32_e32 v217, v175, v120
	v_mov_b32_e32 v218, v217
	v_cvt_pk_bf16_f32 v120, v182, v234
	v_cvt_pk_bf16_f32 v121, v235, v236
	v_cvt_pk_bf16_f32 v122, v237, v238
	v_cvt_pk_bf16_f32 v123, v239, v240
	v_cvt_pk_bf16_f32 v124, v241, v242
	s_waitcnt lgkmcnt(0)
	v_mfma_f32_32x32x16_bf16 v[96:111], v[230:233], v[144:147], v[96:111]
	v_cvt_pk_bf16_f32 v125, v243, v244
	v_cvt_pk_bf16_f32 v126, v245, v246
	v_cvt_pk_bf16_f32 v127, v247, v248
	v_cvt_pk_bf16_f32 v112, v112, v113
	v_cvt_pk_bf16_f32 v113, v114, v115
	v_cvt_pk_bf16_f32 v114, v116, v117
	v_cvt_pk_bf16_f32 v115, v118, v119
	v_cvt_pk_bf16_f32 v116, v168, v169
	v_cvt_pk_bf16_f32 v117, v170, v171
	v_cvt_pk_bf16_f32 v118, v172, v173
	v_cvt_pk_bf16_f32 v119, v174, v175
	v_permlane32_swap_b32_e32 v217, v218
	v_permlane32_swap_b32_e32 v120, v122
	v_permlane32_swap_b32_e32 v121, v123
	v_permlane32_swap_b32_e32 v124, v126
	v_permlane32_swap_b32_e32 v125, v127
	v_permlane32_swap_b32_e32 v112, v114
	v_permlane32_swap_b32_e32 v113, v115
	v_permlane32_swap_b32_e32 v116, v118
	v_permlane32_swap_b32_e32 v117, v119
	s_add_u32 s24, s34, 0x2380c000
	s_addc_u32 s25, s35, 0
	s_add_u32 s34, s34, 0x2380e000
	s_addc_u32 s35, s35, 0
	s_add_u32 s42, s42, 0x21886000
	s_addc_u32 s43, s43, 0
	v_mov_b32_e32 v168, v201
	v_mov_b32_e32 v169, v200
	global_load_dwordx4 v[176:179], v169, s[24:25]
	global_load_dwordx4 v[172:175], v169, s[34:35]
	s_nop 0
	global_load_dwordx4 v[168:171], v168, s[42:43]
	s_and_b64 vcc, exec, s[2:3]
	s_cbranch_vccnz .LBB4_946
	s_mov_b64 s[2:3], s[8:9]
	v_mov_b32_e32 v182, v193
	global_store_dwordx2 v182, v[184:185], s[2:3] nt
